# rows<1>: next row's residual row fetched during the current row's router dot products
# baseline (speedup 1.0000x reference)
; template <int MODE>
; DEVI void phase_rows(const Params& p, int l, char* smem) {
;     ...
;     if (MODE == 1) {
;         const float* rw = p.router_w + (size_t)l * 2048 * 16;
;         f32x4 rwv[16];
; #pragma unroll
;         for (int it = 0; it < 16; ++it) { const int i = tid + it * 512; rwv[it] = *(const f32x4*)(rw + (i >> 2) * 16 + (i & 3) * 4); }
; #pragma unroll
;         for (int it = 0; it < 16; ++it) { const int i = tid + it * 512, k = i >> 2, e4 = (i & 3) * 4; const f32x4 v = rwv[it];
;             wT[(e4 + 0) * 2048 + k] = v[0]; wT[(e4 + 1) * 2048 + k] = v[1]; wT[(e4 + 2) * 2048 + k] = v[2]; wT[(e4 + 3) * 2048 + k] = v[3]; }
;         __syncthreads();
;     }
.LBB0_1039:
	v_readlane_b32 s6, v254, 20
	s_andn2_b64 vcc, exec, s[16:17]
	v_readlane_b32 s7, v254, 21
	s_cbranch_vccnz .LBB0_1099
	s_waitcnt vmcnt(0)
	v_mov_b32_e32 v4, v0
	s_load_dwordx2 s[14:15], s[0:1], 0x70
	v_readlane_b32 s4, v254, 61
	v_readlane_b32 s5, v254, 62
	s_lshl_b32 s52, s4, 15
	s_lshl_b64 s[4:5], s[52:53], 2
	s_waitcnt lgkmcnt(0)
	s_add_u32 s4, s14, s4
	v_lshlrev_b32_e32 v5, 2, v4
	v_lshlrev_b32_e32 v2, 4, v4
	s_addc_u32 s5, s15, s5
	v_and_b32_e32 v2, 48, v2
	v_and_b32_e32 v68, -16, v5
	v_lshl_add_u64 v[66:67], s[4:5], 0, v[2:3]
	v_ashrrev_i32_e32 v69, 31, v68
	v_lshl_add_u64 v[6:7], v[68:69], 2, v[66:67]
	global_load_dwordx4 v[6:9], v[6:7], off
	v_add_u32_e32 v10, 0x800, v68
	v_ashrrev_i32_e32 v11, 31, v10
	v_lshl_add_u64 v[10:11], v[10:11], 2, v[66:67]
	global_load_dwordx4 v[10:13], v[10:11], off
	v_add_u32_e32 v14, 0x1000, v68
	v_ashrrev_i32_e32 v15, 31, v14
	v_lshl_add_u64 v[14:15], v[14:15], 2, v[66:67]
	global_load_dwordx4 v[14:17], v[14:15], off
	v_add_u32_e32 v18, 0x1800, v68
	v_ashrrev_i32_e32 v19, 31, v18
	v_lshl_add_u64 v[18:19], v[18:19], 2, v[66:67]
	global_load_dwordx4 v[18:21], v[18:19], off
	v_add_u32_e32 v22, 0x2000, v68
	v_ashrrev_i32_e32 v23, 31, v22
	v_lshl_add_u64 v[22:23], v[22:23], 2, v[66:67]
	global_load_dwordx4 v[22:25], v[22:23], off
	v_add_u32_e32 v26, 0x2800, v68
	v_ashrrev_i32_e32 v27, 31, v26
	v_lshl_add_u64 v[26:27], v[26:27], 2, v[66:67]
	global_load_dwordx4 v[26:29], v[26:27], off
	v_add_u32_e32 v30, 0x3000, v68
	v_ashrrev_i32_e32 v31, 31, v30
	v_lshl_add_u64 v[30:31], v[30:31], 2, v[66:67]
	global_load_dwordx4 v[30:33], v[30:31], off
	v_add_u32_e32 v34, 0x3800, v68
	v_ashrrev_i32_e32 v35, 31, v34
	v_lshl_add_u64 v[34:35], v[34:35], 2, v[66:67]
	global_load_dwordx4 v[34:37], v[34:35], off
	v_add_u32_e32 v38, 0x4000, v68
	v_ashrrev_i32_e32 v39, 31, v38
	v_lshl_add_u64 v[38:39], v[38:39], 2, v[66:67]
	global_load_dwordx4 v[38:41], v[38:39], off
	v_add_u32_e32 v42, 0x4800, v68
	v_ashrrev_i32_e32 v43, 31, v42
	v_lshl_add_u64 v[42:43], v[42:43], 2, v[66:67]
	global_load_dwordx4 v[42:45], v[42:43], off
	v_add_u32_e32 v46, 0x5000, v68
	v_ashrrev_i32_e32 v47, 31, v46
	v_lshl_add_u64 v[46:47], v[46:47], 2, v[66:67]
	global_load_dwordx4 v[46:49], v[46:47], off
	v_add_u32_e32 v50, 0x5800, v68
	v_ashrrev_i32_e32 v51, 31, v50
	v_lshl_add_u64 v[50:51], v[50:51], 2, v[66:67]
	global_load_dwordx4 v[50:53], v[50:51], off
	v_add_u32_e32 v54, 0x6000, v68
	v_ashrrev_i32_e32 v55, 31, v54
	v_lshl_add_u64 v[54:55], v[54:55], 2, v[66:67]
	global_load_dwordx4 v[54:57], v[54:55], off
	v_add_u32_e32 v58, 0x6800, v68
	v_ashrrev_i32_e32 v59, 31, v58
	v_lshl_add_u64 v[58:59], v[58:59], 2, v[66:67]
	global_load_dwordx4 v[58:61], v[58:59], off
	v_add_u32_e32 v62, 0x7000, v68
	v_ashrrev_i32_e32 v63, 31, v62
	v_lshl_add_u64 v[62:63], v[62:63], 2, v[66:67]
	global_load_dwordx4 v[62:65], v[62:63], off
	v_add_u32_e32 v68, 0x7800, v68
	v_ashrrev_i32_e32 v69, 31, v68
	v_lshl_add_u64 v[66:67], v[68:69], 2, v[66:67]
	global_load_dwordx4 v[66:69], v[66:67], off
	v_lshlrev_b32_e32 v2, 15, v4
	v_and_b32_e32 v2, 0x18000, v2
	v_add_u32_e32 v2, 0, v2
	v_and_b32_e32 v5, -4, v4
	v_add_u32_e32 v5, v2, v5
	v_readlane_b32 s4, v254, 49
	v_readlane_b32 s5, v254, 50
	s_and_b64 s[4:5], s[4:5], exec
	s_movk_i32 s4, 0x2400
	v_ashrrev_i32_e32 v1, 6, v4
	s_cselect_b32 s14, s4, 0x2000
	s_mov_b32 s4, s2
	s_waitcnt vmcnt(15)
	ds_write2st64_b32 v5, v6, v7 offset1:32
	ds_write2st64_b32 v5, v8, v9 offset0:64 offset1:96
	v_add_u32_e32 v5, 0x200, v4
	v_and_b32_e32 v5, -4, v5
	v_add_u32_e32 v5, v2, v5
	s_waitcnt vmcnt(14)
	ds_write2st64_b32 v5, v10, v11 offset1:32
	ds_write2st64_b32 v5, v12, v13 offset0:64 offset1:96
	v_add_u32_e32 v5, 0x400, v4
	v_and_b32_e32 v5, -4, v5
	v_add_u32_e32 v5, v2, v5
	s_waitcnt vmcnt(13)
	ds_write2st64_b32 v5, v14, v15 offset1:32
	ds_write2st64_b32 v5, v16, v17 offset0:64 offset1:96
	v_add_u32_e32 v5, 0x600, v4
	v_and_b32_e32 v5, -4, v5
	v_add_u32_e32 v5, v2, v5
	s_waitcnt vmcnt(12)
	ds_write2st64_b32 v5, v18, v19 offset1:32
	ds_write2st64_b32 v5, v20, v21 offset0:64 offset1:96
	v_add_u32_e32 v5, 0x800, v4
	v_and_b32_e32 v5, -4, v5
	v_add_u32_e32 v5, v2, v5
	s_waitcnt vmcnt(11)
	ds_write2st64_b32 v5, v22, v23 offset1:32
	ds_write2st64_b32 v5, v24, v25 offset0:64 offset1:96
	v_add_u32_e32 v5, 0xa00, v4
	v_and_b32_e32 v5, -4, v5
	v_add_u32_e32 v5, v2, v5
	s_waitcnt vmcnt(10)
	ds_write2st64_b32 v5, v26, v27 offset1:32
	ds_write2st64_b32 v5, v28, v29 offset0:64 offset1:96
	v_add_u32_e32 v5, 0xc00, v4
	v_and_b32_e32 v5, -4, v5
	v_add_u32_e32 v5, v2, v5
	s_waitcnt vmcnt(9)
	ds_write2st64_b32 v5, v30, v31 offset1:32
	ds_write2st64_b32 v5, v32, v33 offset0:64 offset1:96
	v_add_u32_e32 v5, 0xe00, v4
	v_and_b32_e32 v5, -4, v5
	v_add_u32_e32 v5, v2, v5
	s_waitcnt vmcnt(8)
	ds_write2st64_b32 v5, v34, v35 offset1:32
	ds_write2st64_b32 v5, v36, v37 offset0:64 offset1:96
	v_add_u32_e32 v5, 0x1000, v4
	v_and_b32_e32 v5, -4, v5
	v_add_u32_e32 v5, v2, v5
	s_waitcnt vmcnt(7)
	ds_write2st64_b32 v5, v38, v39 offset1:32
	ds_write2st64_b32 v5, v40, v41 offset0:64 offset1:96
	v_add_u32_e32 v5, 0x1200, v4
	v_and_b32_e32 v5, -4, v5
	v_add_u32_e32 v5, v2, v5
	s_waitcnt vmcnt(6)
	ds_write2st64_b32 v5, v42, v43 offset1:32
	ds_write2st64_b32 v5, v44, v45 offset0:64 offset1:96
	v_add_u32_e32 v5, 0x1400, v4
	v_and_b32_e32 v5, -4, v5
	v_add_u32_e32 v5, v2, v5
	s_waitcnt vmcnt(5)
	ds_write2st64_b32 v5, v46, v47 offset1:32
	ds_write2st64_b32 v5, v48, v49 offset0:64 offset1:96
	v_add_u32_e32 v5, 0x1600, v4
	v_and_b32_e32 v5, -4, v5
	v_add_u32_e32 v5, v2, v5
	s_waitcnt vmcnt(4)
	ds_write2st64_b32 v5, v50, v51 offset1:32
	ds_write2st64_b32 v5, v52, v53 offset0:64 offset1:96
	v_add_u32_e32 v5, 0x1800, v4
	v_and_b32_e32 v5, -4, v5
	v_add_u32_e32 v5, v2, v5
	s_waitcnt vmcnt(3)
	ds_write2st64_b32 v5, v54, v55 offset1:32
	ds_write2st64_b32 v5, v56, v57 offset0:64 offset1:96
	v_add_u32_e32 v5, 0x1a00, v4
	v_and_b32_e32 v5, -4, v5
	v_add_u32_e32 v5, v2, v5
	s_waitcnt vmcnt(2)
	ds_write2st64_b32 v5, v58, v59 offset1:32
	ds_write2st64_b32 v5, v60, v61 offset0:64 offset1:96
	v_add_u32_e32 v5, 0x1c00, v4
	v_and_b32_e32 v5, -4, v5
	v_add_u32_e32 v5, v2, v5
	s_waitcnt vmcnt(1)
	ds_write2st64_b32 v5, v62, v63 offset1:32
	ds_write2st64_b32 v5, v64, v65 offset0:64 offset1:96
	v_add_u32_e32 v5, 0x1e00, v4
	v_and_b32_e32 v5, -4, v5
	v_add_u32_e32 v2, v2, v5
	s_waitcnt vmcnt(0)
	ds_write2st64_b32 v2, v66, v67 offset1:32
	ds_write2st64_b32 v2, v68, v69 offset0:64 offset1:96
	s_waitcnt lgkmcnt(0)
	s_barrier
; DEVI int obid() { int b = blockIdx.x; asm volatile("" : "+s"(b)); return b; }
; template <int MODE>
; DEVI void phase_rows(const Params& p, int l, char* smem) {
;     ...
;     for (int row = obid() * 8 + wid; row < nrows; row += gridDim.x * 8) {
;         const bool lat = row < NLAT;
;         const int b = lat ? (row >> 11) : ((row - NLAT) >> 8);
;         const int tok = lat ? (row & 2047) : (SEQ + ((row - NLAT) & 255));
;         float v[32];
;         if (MODE == 0) { const float* src = lat ? p.x + (size_t)row * DM : p.ctx + (size_t)(row - NLAT) * DM;
; #pragma unroll
;             for (int i = 0; i < 8; ++i) { const f32x4 t = *(const f32x4*)(src + i * 256 + lane * 4); v[i * 4] = t[0]; v[i * 4 + 1] = t[1]; v[i * 4 + 2] = t[2]; v[i * 4 + 3] = t[3]; }
;         } else { const bf16_t* src = xres + (size_t)row * DM;
;     ...
;                 for (int i = 0; i < 8; ++i) { const f32x4 w = *(const f32x4*)(wT + e * 2048 + i * 256 + lane * 4);
;                     t += v[i * 4] * w[0] + v[i * 4 + 1] * w[1] + v[i * 4 + 2] * w[2] + v[i * 4 + 3] * w[3]; }
;                 a[e] = t; if ((e & 3) == 3) __builtin_amdgcn_sched_barrier(0); }
;             const bool b5 = (lane & 32) != 0, b4 = (lane & 16) != 0, b3 = (lane & 8) != 0, b2 = (lane & 4) != 0;
;             float s8[8], s4[4], s2[2], s1;
; #pragma unroll
;             for (int i = 0; i < 8; ++i) { const float keep = b5 ? a[8 + i] : a[i], give = b5 ? a[i] : a[8 + i]; s8[i] = keep + __shfl_xor(give, 32); }
; #pragma unroll
;             for (int i = 0; i < 4; ++i) { const float keep = b4 ? s8[4 + i] : s8[i], give = b4 ? s8[i] : s8[4 + i]; s4[i] = keep + __shfl_xor(give, 16); }
; #pragma unroll
;             for (int i = 0; i < 2; ++i) { const float keep = b3 ? s4[2 + i] : s4[i], give = b3 ? s4[i] : s4[2 + i]; s2[i] = keep + __shfl_xor(give, 8); }
;             { const float keep = b2 ? s2[1] : s2[0], give = b2 ? s2[0] : s2[1]; s1 = keep + __shfl_xor(give, 4); }
;             s1 += __shfl_xor(s1, 2); s1 += __shfl_xor(s1, 1);
;             float mx = s1;
; #pragma unroll
;             for (int off = 32; off >= 4; off >>= 1) mx = fmaxf(mx, __shfl_xor(mx, off));
;             const float ex = expf(s1 - mx); float den = ex;
; #pragma unroll
;             for (int off = 32; off >= 4; off >>= 1) den += __shfl_xor(den, off);
;             const int eidx = (b5 ? 8 : 0) + (b4 ? 4 : 0) + (b3 ? 2 : 0) + (b2 ? 1 : 0);
	s_nop 0
	v_lshl_add_u32 v68, s4, 3, v1
	v_cmp_gt_i32_e32 vcc, s14, v68
	s_and_saveexec_b64 s[54:55], vcc
	s_cbranch_execz .LBB0_1045
	v_and_b32_e32 v5, 63, v4
	v_lshlrev_b32_e32 v6, 3, v5
	v_mov_b32_e32 v7, v3
	v_and_b32_e32 v1, 64, v227
	v_lshl_add_u64 v[70:71], s[26:27], 0, v[6:7]
	v_add_u32_e32 v6, 64, v1
	v_xor_b32_e32 v1, 32, v227
	v_cmp_lt_i32_e32 vcc, v1, v6
	v_xor_b32_e32 v7, 16, v227
	v_readlane_b32 s4, v253, 2
	v_cndmask_b32_e32 v1, v227, v1, vcc
	v_cmp_lt_i32_e32 vcc, v7, v6
	v_lshlrev_b32_e32 v2, 2, v5
	v_readlane_b32 s5, v253, 3
	v_cndmask_b32_e32 v7, v227, v7, vcc
	v_lshlrev_b32_e32 v75, 2, v7
	v_xor_b32_e32 v7, 8, v227
	v_cmp_lt_i32_e32 vcc, v7, v6
	v_lshl_add_u64 v[72:73], s[4:5], 0, v[2:3]
	v_lshl_add_u32 v86, v5, 4, 0
	v_cndmask_b32_e32 v7, v227, v7, vcc
	v_lshlrev_b32_e32 v82, 2, v7
	v_xor_b32_e32 v7, 4, v227
	v_cmp_lt_i32_e32 vcc, v7, v6
	v_and_b32_e32 v5, 32, v4
	s_load_dword s4, s[66:67], 0x0
	v_cndmask_b32_e32 v7, v227, v7, vcc
	v_lshlrev_b32_e32 v83, 2, v7
	v_xor_b32_e32 v7, 2, v227
	v_cmp_lt_i32_e32 vcc, v7, v6
	v_cmp_eq_u32_e64 s[38:39], 0, v5
	v_and_b32_e32 v5, 16, v4
	v_cndmask_b32_e32 v7, v227, v7, vcc
	v_lshlrev_b32_e32 v84, 2, v7
	v_xor_b32_e32 v7, 1, v227
	v_cmp_eq_u32_e64 s[40:41], 0, v5
	v_and_b32_e32 v5, 8, v4
	v_cmp_lt_i32_e32 vcc, v7, v6
	v_cmp_eq_u32_e64 s[42:43], 0, v5
	v_and_b32_e32 v5, 4, v4
	v_cndmask_b32_e32 v6, v227, v7, vcc
	v_cmp_eq_u32_e64 s[44:45], 0, v5
	v_and_b32_e32 v5, 3, v4
	v_lshlrev_b32_e32 v1, 2, v1
	v_lshlrev_b32_e32 v85, 2, v6
	v_cmp_eq_u32_e64 s[46:47], 0, v5
	v_bfe_u32 v74, v4, 2, 4
	s_waitcnt lgkmcnt(0)
	s_lshl_b32 s15, s4, 3
	v_add_u32_e32 v87, 0x10000, v86
	v_add_u32_e32 v88, 0x10400, v86
	v_add_u32_e32 v89, 0x10800, v86
	v_add_u32_e32 v90, 0x10c00, v86
	v_add_u32_e32 v91, 0x11000, v86
	v_add_u32_e32 v92, 0x11400, v86
	v_add_u32_e32 v93, 0x11800, v86
	v_add_u32_e32 v94, 0x11c00, v86
	v_add_u32_e32 v95, 0x13c00, v86
	v_add_u32_e32 v96, 0x12000, v86
	v_add_u32_e32 v97, 0x13800, v86
	v_add_u32_e32 v98, 0x13400, v86
	v_add_u32_e32 v99, 0x13000, v86
	v_add_u32_e32 v100, 0x12c00, v86
	v_add_u32_e32 v101, 0x12800, v86
	v_add_u32_e32 v102, 0x12400, v86
	v_add_u32_e32 v103, 0x15c00, v86
	v_add_u32_e32 v104, 0x14000, v86
	v_add_u32_e32 v105, 0x15800, v86
	v_add_u32_e32 v106, 0x15400, v86
	v_add_u32_e32 v107, 0x15000, v86
	v_add_u32_e32 v108, 0x14c00, v86
	v_add_u32_e32 v109, 0x14800, v86
	v_add_u32_e32 v110, 0x14400, v86
	v_add_u32_e32 v111, 0x17c00, v86
	v_add_u32_e32 v112, 0x16000, v86
	v_add_u32_e32 v113, 0x17800, v86
	v_add_u32_e32 v114, 0x17400, v86
	v_add_u32_e32 v115, 0x17000, v86
	v_add_u32_e32 v116, 0x16c00, v86
	v_add_u32_e32 v117, 0x16800, v86
	v_add_u32_e32 v118, 0x16400, v86
	v_add_u32_e32 v119, 0x18000, v86
	v_add_u32_e32 v120, 0x18400, v86
	v_add_u32_e32 v121, 0x18800, v86
	v_add_u32_e32 v122, 0x18c00, v86
	v_add_u32_e32 v123, 0x19000, v86
	v_add_u32_e32 v124, 0x19400, v86
	v_add_u32_e32 v125, 0x19800, v86
	v_add_u32_e32 v126, 0x19c00, v86
	v_add_u32_e32 v127, 0x1bc00, v86
	v_add_u32_e32 v128, 0x1a000, v86
	v_add_u32_e32 v129, 0x1b800, v86
	v_add_u32_e32 v130, 0x1b400, v86
	v_add_u32_e32 v131, 0x1b000, v86
	v_add_u32_e32 v132, 0x1ac00, v86
	v_add_u32_e32 v133, 0x1a800, v86
	v_add_u32_e32 v134, 0x1a400, v86
	v_add_u32_e32 v135, 0x1dc00, v86
	v_add_u32_e32 v136, 0x1c000, v86
	v_add_u32_e32 v137, 0x1d800, v86
	v_add_u32_e32 v138, 0x1d400, v86
	v_add_u32_e32 v139, 0x1d000, v86
	v_add_u32_e32 v140, 0x1cc00, v86
	v_add_u32_e32 v141, 0x1c800, v86
	v_add_u32_e32 v142, 0x1c400, v86
	v_add_u32_e32 v143, 0x1fc00, v86
	v_add_u32_e32 v144, 0x1e000, v86
	v_add_u32_e32 v145, 0x1f800, v86
	v_add_u32_e32 v146, 0x1f400, v86
	v_add_u32_e32 v147, 0x1f000, v86
	v_add_u32_e32 v148, 0x1ec00, v86
	v_add_u32_e32 v149, 0x1e800, v86
	v_add_u32_e32 v150, 0x1e400, v86
	s_mov_b64 s[56:57], 0
	v_lshlrev_b32_e32 v2, 2, v2
	v_lshlrev_b32_e32 v236, 12, v68
	v_mov_b32_e32 v237, 0
	v_lshl_add_u64 v[236:237], v[70:71], 0, v[236:237]
	global_load_dwordx2 v[210:211], v[236:237], off
	global_load_dwordx2 v[212:213], v[236:237], off offset:3584
	global_load_dwordx2 v[214:215], v[236:237], off offset:512
	global_load_dwordx2 v[216:217], v[236:237], off offset:1024
	global_load_dwordx2 v[218:219], v[236:237], off offset:1536
	global_load_dwordx2 v[220:221], v[236:237], off offset:2048
	global_load_dwordx2 v[228:229], v[236:237], off offset:2560
	global_load_dwordx2 v[232:233], v[236:237], off offset:3072
	s_waitcnt vmcnt(0)
	s_branch .LBB0_1043

; DEVI float bflo(unsigned w) { return __uint_as_float(w << 16); }
; DEVI float bfhi(unsigned w) { return __uint_as_float(w & 0xffff0000u); }
; template <int MODE>
; DEVI void phase_rows(const Params& p, int l, char* smem) {
;     ...
;         } else { const bf16_t* src = xres + (size_t)row * DM;
; #pragma unroll
;             for (int i = 0; i < 8; ++i) { const u32x2 t = *(const u32x2*)(src + i * 256 + lane * 4); v[i * 4] = bflo(t[0]); v[i * 4 + 1] = bfhi(t[0]); v[i * 4 + 2] = bflo(t[1]); v[i * 4 + 3] = bfhi(t[1]); }
;     ...
;         f32x4 shv[8], scv[8];
;         if (MODE != 3) { const float* mr2 = (MODE == 2) ? mrow + (size_t)5 * 12288 : mrow;
;             const float* sh = mr2 + ((MODE == 1) ? 6144 : 0); const float* sc = mr2 + ((MODE == 1) ? 8192 : 2048);
; #pragma unroll
;             for (int i = 0; i < 8; ++i) { shv[i] = *(const f32x4*)(sh + i * 256 + lane * 4); scv[i] = *(const f32x4*)(sc + i * 256 + lane * 4); } }
;         float ss = 0.f;
; #pragma unroll
;         for (int i = 0; i < 32; ++i) ss += v[i] * v[i];
;         ss = wave_sum(ss);
;         const float rstd = rsqrtf(ss * (1.f / DM) + EPS);
.LBB0_1043:
	v_ashrrev_i32_e32 v69, 31, v68
	v_lshlrev_b64 v[4:5], 12, v[68:69]
	v_lshl_add_u64 v[4:5], v[70:71], 0, v[4:5]
	s_waitcnt lgkmcnt(0)
	s_waitcnt vmcnt(1)
	v_mov_b64_e32 v[6:7], v[210:211]
	v_mov_b64_e32 v[78:79], v[212:213]
	v_mov_b64_e32 v[198:199], v[214:215]
	v_mov_b64_e32 v[200:201], v[216:217]
	v_mov_b64_e32 v[202:203], v[218:219]
	v_mov_b64_e32 v[204:205], v[220:221]
	v_mov_b64_e32 v[206:207], v[228:229]
	v_mov_b64_e32 v[208:209], v[232:233]
	v_cmp_gt_i32_e32 vcc, s90, v68
	v_ashrrev_i32_e32 v151, 11, v68
	v_readlane_b32 s4, v254, 61
	v_readlane_b32 s5, v254, 62
	s_mul_i32 s4, s4, 5
	v_lshlrev_b64 v[80:81], 11, v[68:69]
	v_lshl_add_u64 v[80:81], v[72:73], 0, v[80:81]
	s_waitcnt vmcnt(7)
	v_lshlrev_b32_e32 v179, 16, v6
	v_and_b32_e32 v178, 0xffff0000, v6
	v_lshlrev_b32_e32 v177, 16, v7
	v_and_b32_e32 v176, 0xffff0000, v7
	v_mul_f32_e32 v175, v178, v178
	v_fmac_f32_e32 v175, v179, v179
	v_fmac_f32_e32 v175, v177, v177
	v_fmac_f32_e32 v175, v176, v176
	s_waitcnt vmcnt(6)
	v_and_b32_e32 v76, 0xffff0000, v78
	v_lshlrev_b32_e32 v77, 16, v78
	v_pk_mul_f32 v[180:181], v[76:77], v[76:77]
	s_waitcnt vmcnt(5)
	v_mov_b64_e32 v[6:7], v[198:199]
	v_lshlrev_b32_e32 v174, 16, v6
	v_and_b32_e32 v173, 0xffff0000, v6
	v_lshlrev_b32_e32 v172, 16, v7
	v_and_b32_e32 v171, 0xffff0000, v7
	v_fmac_f32_e32 v175, v174, v174
	v_fmac_f32_e32 v175, v173, v173
	v_fmac_f32_e32 v175, v172, v172
	v_fmac_f32_e32 v175, v171, v171
	s_waitcnt vmcnt(4)
	v_mov_b64_e32 v[6:7], v[200:201]
	v_lshlrev_b32_e32 v170, 16, v6
	v_and_b32_e32 v169, 0xffff0000, v6
	v_lshlrev_b32_e32 v168, 16, v7
	v_and_b32_e32 v167, 0xffff0000, v7
	v_fmac_f32_e32 v175, v170, v170
	v_fmac_f32_e32 v175, v169, v169
	v_fmac_f32_e32 v175, v168, v168
	v_fmac_f32_e32 v175, v167, v167
	s_waitcnt vmcnt(3)
	v_mov_b64_e32 v[6:7], v[202:203]
	v_lshlrev_b32_e32 v166, 16, v6
	v_and_b32_e32 v165, 0xffff0000, v6
	v_lshlrev_b32_e32 v164, 16, v7
	v_and_b32_e32 v163, 0xffff0000, v7
	v_fmac_f32_e32 v175, v166, v166
	v_fmac_f32_e32 v175, v165, v165
	v_fmac_f32_e32 v175, v164, v164
	v_fmac_f32_e32 v175, v163, v163
	s_waitcnt vmcnt(2)
	v_mov_b64_e32 v[6:7], v[204:205]
	v_lshlrev_b32_e32 v162, 16, v6
	v_and_b32_e32 v161, 0xffff0000, v6
	v_lshlrev_b32_e32 v160, 16, v7
	v_and_b32_e32 v159, 0xffff0000, v7
	v_fmac_f32_e32 v175, v162, v162
	v_fmac_f32_e32 v175, v161, v161
	v_fmac_f32_e32 v175, v160, v160
	v_fmac_f32_e32 v175, v159, v159
	s_waitcnt vmcnt(1)
	v_mov_b64_e32 v[6:7], v[206:207]
	v_lshlrev_b32_e32 v158, 16, v6
	v_and_b32_e32 v157, 0xffff0000, v6
	v_lshlrev_b32_e32 v156, 16, v7
	v_and_b32_e32 v155, 0xffff0000, v7
	v_cndmask_b32_e32 v4, 4, v151, vcc
	v_add_u32_e32 v4, s4, v4
	v_readlane_b32 s4, v254, 18
	v_mul_hi_i32_i24_e32 v5, 0xc000, v4
	v_mul_i32_i24_e32 v4, 0xc000, v4
	v_readlane_b32 s5, v254, 19
	v_fmac_f32_e32 v175, v158, v158
	v_fmac_f32_e32 v175, v157, v157
	v_lshl_add_u64 v[4:5], s[4:5], 0, v[4:5]
	v_lshl_add_u64 v[4:5], v[4:5], 0, v[2:3]
	s_mov_b64 s[4:5], 0x6000
	v_lshl_add_u64 v[8:9], v[4:5], 0, s[74:75]
	v_fmac_f32_e32 v175, v156, v156
	v_fmac_f32_e32 v175, v155, v155
	s_waitcnt vmcnt(0)
	v_mov_b64_e32 v[6:7], v[208:209]
	v_lshlrev_b32_e32 v154, 16, v6
	v_and_b32_e32 v153, 0xffff0000, v6
	v_lshlrev_b32_e32 v152, 16, v7
	v_and_b32_e32 v69, 0xffff0000, v7
	v_lshl_add_u64 v[6:7], v[4:5], 0, s[4:5]
	s_movk_i32 s4, 0x7000
	v_add_co_u32_e64 v36, s[50:51], s4, v4
	s_mov_b32 s4, 0x9000
	s_nop 0
	v_addc_co_u32_e64 v37, s[50:51], 0, v5, s[50:51]
	global_load_dwordx4 v[20:23], v[36:37], off offset:-4096
	v_add_co_u32_e64 v38, s[50:51], s4, v4
	v_fmac_f32_e32 v175, v154, v154
	s_nop 0
	v_addc_co_u32_e64 v39, s[50:51], 0, v5, s[50:51]
	global_load_dwordx4 v[64:67], v[38:39], off offset:-4096
	global_load_dwordx4 v[28:31], v[6:7], off offset:1024
	global_load_dwordx4 v[60:63], v[8:9], off offset:1024
	global_load_dwordx4 v[32:35], v[6:7], off offset:2048
	global_load_dwordx4 v[56:59], v[8:9], off offset:2048
	global_load_dwordx4 v[24:27], v[6:7], off offset:3072
	global_load_dwordx4 v[52:55], v[8:9], off offset:3072
	global_load_dwordx4 v[16:19], v[36:37], off
	global_load_dwordx4 v[48:51], v[38:39], off
	global_load_dwordx4 v[12:15], v[36:37], off offset:1024
	global_load_dwordx4 v[44:47], v[38:39], off offset:1024
	s_nop 0
	global_load_dwordx4 v[8:11], v[36:37], off offset:2048
	global_load_dwordx4 v[40:43], v[38:39], off offset:2048
	global_load_dwordx4 v[4:7], v[36:37], off offset:3072
	s_nop 0
	global_load_dwordx4 v[36:39], v[38:39], off offset:3072
	v_fmac_f32_e32 v175, v153, v153
	v_fmac_f32_e32 v175, v152, v152
	v_fmac_f32_e32 v175, v69, v69
	v_add_f32_e32 v78, v181, v175
	v_add_f32_e32 v175, v180, v78
	v_and_b32_e32 v78, 0xffff0000, v79
	v_lshlrev_b32_e32 v79, 16, v79
	v_pk_mul_f32 v[180:181], v[78:79], v[78:79]
	s_waitcnt vmcnt(14)
	v_add_f32_e32 v64, 1.0, v64
	v_add_f32_e32 v175, v181, v175
	v_add_f32_e32 v175, v180, v175
	ds_bpermute_b32 v180, v1, v175
	v_add_f32_e32 v65, 1.0, v65
	s_waitcnt vmcnt(12)
	v_add_f32_e32 v60, 1.0, v60
	s_waitcnt vmcnt(10)
	v_add_f32_e32 v56, 1.0, v56
	s_waitcnt vmcnt(8)
	v_add_f32_e32 v52, 1.0, v52
	s_waitcnt lgkmcnt(0)
	v_add_f32_e32 v175, v175, v180
	ds_bpermute_b32 v180, v75, v175
	s_waitcnt vmcnt(6)
	v_add_f32_e32 v48, 1.0, v48
	s_waitcnt vmcnt(4)
	v_add_f32_e32 v44, 1.0, v44
	s_waitcnt vmcnt(2)
	v_add_f32_e32 v40, 1.0, v40
	s_waitcnt lgkmcnt(0)
	v_add_f32_e32 v175, v175, v180
	ds_bpermute_b32 v180, v82, v175
	s_waitcnt vmcnt(0)
	v_add_f32_e32 v36, 1.0, v36
	s_waitcnt lgkmcnt(0)
	v_add_f32_e32 v175, v175, v180
	ds_bpermute_b32 v180, v83, v175
	s_waitcnt lgkmcnt(0)
	v_add_f32_e32 v175, v175, v180
	ds_bpermute_b32 v180, v84, v175
	s_waitcnt lgkmcnt(0)
; DEVI unsigned cvt_pk(float lo, float hi) { f32x2 v = {lo, hi}; bf16x2_t b = __builtin_convertvector(v, bf16x2_t); return __builtin_bit_cast(unsigned, b); }
; DEVI unsigned cvt4_fp8c(float a, float b, float c, float d) { return cvt4_fp8(clamp8(a), clamp8(b), clamp8(c), clamp8(d)); }
; template <int MODE>
; DEVI void phase_rows(const Params& p, int l, char* smem) {
;     ...
;         const float rstd = rsqrtf(ss * (1.f / DM) + EPS);
;         if (MODE == 3) {
; #pragma unroll
;             for (int i = 0; i < 8; ++i) { const f32x4 g = *(const f32x4*)(p.final_norm + i * 256 + lane * 4);
;                 __builtin_nontemporal_store((f32x4){v[i * 4] * rstd * g[0], v[i * 4 + 1] * rstd * g[1], v[i * 4 + 2] * rstd * g[2], v[i * 4 + 3] * rstd * g[3]}, (f32x4*)(p.out + (size_t)row * DM + i * 256 + lane * 4)); }
;             continue;
;         }
; #pragma unroll
;         for (int i = 0; i < 8; ++i) { const f32x4 a = shv[i]; const f32x4 s = scv[i];
; #pragma unroll
;             for (int j = 0; j < 4; ++j) v[i * 4 + j] = v[i * 4 + j] * rstd * (1.f + s[j]) + a[j];
;             if (MODE == 1) *(unsigned*)((unsigned char*)hbuf + (size_t)row * DM + i * 256 + lane * 4) = cvt4_fp8c(v[i * 4], v[i * 4 + 1], v[i * 4 + 2], v[i * 4 + 3]);
;             else *(u32x2*)(hbuf + (size_t)row * DM + i * 256 + lane * 4) = (u32x2){cvt_pk(v[i * 4], v[i * 4 + 1]), cvt_pk(v[i * 4 + 2], v[i * 4 + 3])}; }
;         if (MODE == 1) {
;             float a[16];
; #pragma unroll
;             for (int e = 0; e < 16; ++e) { float t = 0.f;
; #pragma unroll
;                 for (int i = 0; i < 8; ++i) { const f32x4 w = *(const f32x4*)(wT + e * 2048 + i * 256 + lane * 4);
;                     t += v[i * 4] * w[0] + v[i * 4 + 1] * w[1] + v[i * 4 + 2] * w[2] + v[i * 4 + 3] * w[3]; }
	v_add_f32_e32 v175, v175, v180
	ds_bpermute_b32 v180, v85, v175
	s_waitcnt lgkmcnt(0)
	v_add_f32_e32 v175, v175, v180
	v_fmamk_f32 v175, v175, 0x3a000000, v223
	v_cmp_gt_f32_e64 s[50:51], s97, v175
	v_mul_f32_e32 v180, 0x4b800000, v175
	s_nop 0
	v_cndmask_b32_e64 v175, v175, v180, s[50:51]
	v_rsq_f32_e32 v175, v175
	s_nop 0
	v_mul_f32_e32 v180, 0x45800000, v175
	v_cndmask_b32_e64 v175, v175, v180, s[50:51]
	v_mul_f32_e32 v179, v175, v179
	v_fma_f32 v20, v64, v179, v20
	v_mul_f32_e32 v64, v175, v178
	v_fma_f32 v64, v65, v64, v21
	v_mul_f32_e32 v21, v175, v177
	v_add_f32_e32 v65, 1.0, v66
	v_fma_f32 v21, v65, v21, v22
	v_mul_f32_e32 v22, v175, v176
	v_add_f32_e32 v65, 1.0, v67
	v_fmac_f32_e32 v23, v65, v22
	v_med3_f32 v22, v20, s89, v238
	v_med3_f32 v65, v64, s89, v238
	v_mov_b32_e32 v176, v3
	v_cvt_pk_fp8_f32 v176, v22, v65
	v_mul_f32_e32 v22, v175, v174
	v_fma_f32 v22, v60, v22, v28
	v_mul_f32_e32 v28, v175, v173
	v_add_f32_e32 v60, 1.0, v61
	v_fma_f32 v29, v60, v28, v29
	v_mul_f32_e32 v28, v175, v172
	v_add_f32_e32 v60, 1.0, v62
	v_fma_f32 v28, v60, v28, v30
	v_mul_f32_e32 v30, v175, v171
	v_add_f32_e32 v60, 1.0, v63
	v_fmac_f32_e32 v31, v60, v30
	v_med3_f32 v30, v22, s89, v238
	v_med3_f32 v60, v29, s89, v238
	v_mov_b32_e32 v63, v3
	v_cvt_pk_fp8_f32 v63, v30, v60
	v_mul_f32_e32 v30, v175, v170
	v_fma_f32 v30, v56, v30, v32
	v_mul_f32_e32 v32, v175, v169
	v_add_f32_e32 v56, 1.0, v57
	v_fma_f32 v33, v56, v32, v33
	v_mul_f32_e32 v32, v175, v168
	v_add_f32_e32 v56, 1.0, v58
	v_fma_f32 v32, v56, v32, v34
	v_mul_f32_e32 v34, v175, v167
	v_add_f32_e32 v56, 1.0, v59
	v_fmac_f32_e32 v35, v56, v34
	v_med3_f32 v34, v30, s89, v238
	v_med3_f32 v56, v33, s89, v238
	v_mov_b32_e32 v59, v3
	v_cvt_pk_fp8_f32 v59, v34, v56
	v_mul_f32_e32 v34, v175, v166
	v_fma_f32 v24, v52, v34, v24
	v_mul_f32_e32 v34, v175, v165
	v_add_f32_e32 v52, 1.0, v53
	v_fma_f32 v34, v52, v34, v25
	v_mul_f32_e32 v25, v175, v164
	v_add_f32_e32 v52, 1.0, v54
	v_fma_f32 v25, v52, v25, v26
	v_mul_f32_e32 v26, v175, v163
	v_add_f32_e32 v52, 1.0, v55
	v_fmac_f32_e32 v27, v52, v26
	v_med3_f32 v26, v24, s89, v238
	v_med3_f32 v52, v34, s89, v238
	v_mov_b32_e32 v55, v3
	v_cvt_pk_fp8_f32 v55, v26, v52
	v_mul_f32_e32 v26, v175, v162
	v_fma_f32 v16, v48, v26, v16
	v_mul_f32_e32 v26, v175, v161
	v_add_f32_e32 v48, 1.0, v49
	v_fma_f32 v26, v48, v26, v17
	v_mul_f32_e32 v17, v175, v160
	v_add_f32_e32 v48, 1.0, v50
	v_fma_f32 v17, v48, v17, v18
	v_mul_f32_e32 v18, v175, v159
	v_add_f32_e32 v48, 1.0, v51
	v_fmac_f32_e32 v19, v48, v18
	v_med3_f32 v18, v16, s89, v238
	v_med3_f32 v48, v26, s89, v238
	v_mov_b32_e32 v51, v3
	v_cvt_pk_fp8_f32 v51, v18, v48
	v_mul_f32_e32 v18, v175, v158
	v_fma_f32 v12, v44, v18, v12
	v_mul_f32_e32 v18, v175, v157
	v_add_f32_e32 v44, 1.0, v45
	v_fma_f32 v18, v44, v18, v13
	v_mul_f32_e32 v13, v175, v156
	v_add_f32_e32 v44, 1.0, v46
	v_fma_f32 v13, v44, v13, v14
	v_mul_f32_e32 v14, v175, v155
	v_add_f32_e32 v44, 1.0, v47
	v_fmac_f32_e32 v15, v44, v14
	v_med3_f32 v14, v12, s89, v238
	v_med3_f32 v44, v18, s89, v238
	v_mov_b32_e32 v47, v3
	v_cvt_pk_fp8_f32 v47, v14, v44
	v_mul_f32_e32 v14, v175, v154
	v_fma_f32 v8, v40, v14, v8
	v_mul_f32_e32 v14, v175, v153
	v_add_f32_e32 v40, 1.0, v41
	v_fma_f32 v14, v40, v14, v9
	v_mul_f32_e32 v9, v175, v152
	v_add_f32_e32 v40, 1.0, v42
	v_fma_f32 v9, v40, v9, v10
	v_mul_f32_e32 v10, v175, v69
	v_add_f32_e32 v40, 1.0, v43
	v_fmac_f32_e32 v11, v40, v10
	v_med3_f32 v10, v8, s89, v238
	v_med3_f32 v40, v14, s89, v238
	v_mov_b32_e32 v43, v3
	v_cvt_pk_fp8_f32 v43, v10, v40
	v_mul_f32_e32 v10, v175, v77
	v_fma_f32 v4, v36, v10, v4
	v_mul_f32_e32 v10, v175, v76
	v_add_f32_e32 v36, 1.0, v37
	v_fma_f32 v10, v36, v10, v5
	v_mul_f32_e32 v5, v175, v79
	v_add_f32_e32 v36, 1.0, v38
	v_fma_f32 v5, v36, v5, v6
	v_mul_f32_e32 v6, v175, v78
	v_add_f32_e32 v36, 1.0, v39
	v_fmac_f32_e32 v7, v36, v6
	v_med3_f32 v6, v4, s89, v238
	v_med3_f32 v36, v10, s89, v238
	v_mov_b32_e32 v39, v3
	v_cvt_pk_fp8_f32 v39, v6, v36
	v_med3_f32 v37, v5, s89, v238
	v_med3_f32 v38, v7, s89, v238
	v_med3_f32 v66, v21, s89, v238
	v_cvt_pk_fp8_f32 v39, v37, v38 op_sel:[0,0,1]
	v_med3_f32 v67, v23, s89, v238
	v_med3_f32 v61, v28, s89, v238
	v_med3_f32 v62, v31, s89, v238
	global_store_dword v[80:81], v39, off offset:1792
	ds_read_b128 v[36:39], v86
	v_med3_f32 v57, v32, s89, v238
	v_med3_f32 v58, v35, s89, v238
	v_med3_f32 v53, v25, s89, v238
	v_med3_f32 v54, v27, s89, v238
	s_waitcnt lgkmcnt(0)
	v_mul_f32_e32 v6, v64, v37
	v_fmac_f32_e32 v6, v20, v36
	v_fmac_f32_e32 v6, v21, v38
	v_fmac_f32_e32 v6, v23, v39
	ds_read_b128 v[36:39], v86 offset:1024
	v_add_f32_e32 v6, 0, v6
	v_med3_f32 v49, v17, s89, v238
	v_med3_f32 v50, v19, s89, v238
	v_med3_f32 v45, v13, s89, v238
	s_waitcnt lgkmcnt(0)
	v_mul_f32_e32 v37, v29, v37
	v_fmac_f32_e32 v37, v22, v36
	v_fmac_f32_e32 v37, v28, v38
	v_fmac_f32_e32 v37, v31, v39
	v_add_f32_e32 v6, v6, v37
	ds_read_b128 v[36:39], v86 offset:2048
	v_med3_f32 v46, v15, s89, v238
	v_med3_f32 v41, v9, s89, v238
	v_med3_f32 v42, v11, s89, v238
	v_cvt_pk_fp8_f32 v176, v66, v67 op_sel:[0,0,1]
	s_waitcnt lgkmcnt(0)
	v_mul_f32_e32 v37, v33, v37
	v_fmac_f32_e32 v37, v30, v36
	v_fmac_f32_e32 v37, v32, v38
	v_fmac_f32_e32 v37, v35, v39
	v_add_f32_e32 v6, v6, v37
	ds_read_b128 v[36:39], v86 offset:3072
	v_cvt_pk_fp8_f32 v63, v61, v62 op_sel:[0,0,1]
	v_cvt_pk_fp8_f32 v59, v57, v58 op_sel:[0,0,1]
	v_cvt_pk_fp8_f32 v55, v53, v54 op_sel:[0,0,1]
	v_cvt_pk_fp8_f32 v51, v49, v50 op_sel:[0,0,1]
	s_waitcnt lgkmcnt(0)
; DEVI unsigned cvt_pk(float lo, float hi) { f32x2 v = {lo, hi}; bf16x2_t b = __builtin_convertvector(v, bf16x2_t); return __builtin_bit_cast(unsigned, b); }
; DEVI unsigned cvt4_fp8c(float a, float b, float c, float d) { return cvt4_fp8(clamp8(a), clamp8(b), clamp8(c), clamp8(d)); }
; template <int MODE>
; DEVI void phase_rows(const Params& p, int l, char* smem) {
;     ...
;             if (MODE == 1) *(unsigned*)((unsigned char*)hbuf + (size_t)row * DM + i * 256 + lane * 4) = cvt4_fp8c(v[i * 4], v[i * 4 + 1], v[i * 4 + 2], v[i * 4 + 3]);
;             else *(u32x2*)(hbuf + (size_t)row * DM + i * 256 + lane * 4) = (u32x2){cvt_pk(v[i * 4], v[i * 4 + 1]), cvt_pk(v[i * 4 + 2], v[i * 4 + 3])}; }
;         if (MODE == 1) {
;             float a[16];
; #pragma unroll
;             for (int e = 0; e < 16; ++e) { float t = 0.f;
; #pragma unroll
;                 for (int i = 0; i < 8; ++i) { const f32x4 w = *(const f32x4*)(wT + e * 2048 + i * 256 + lane * 4);
;                     t += v[i * 4] * w[0] + v[i * 4 + 1] * w[1] + v[i * 4 + 2] * w[2] + v[i * 4 + 3] * w[3]; }
;                 a[e] = t; if ((e & 3) == 3) __builtin_amdgcn_sched_barrier(0); }
	v_mul_f32_e32 v37, v34, v37
	v_fmac_f32_e32 v37, v24, v36
	v_fmac_f32_e32 v37, v25, v38
	v_fmac_f32_e32 v37, v27, v39
	v_add_f32_e32 v6, v6, v37
	ds_read_b128 v[36:39], v86 offset:4096
	v_cvt_pk_fp8_f32 v47, v45, v46 op_sel:[0,0,1]
	v_cvt_pk_fp8_f32 v43, v41, v42 op_sel:[0,0,1]
	global_store_dword v[80:81], v176, off
	global_store_dword v[80:81], v63, off offset:256
	s_waitcnt lgkmcnt(0)
	v_mul_f32_e32 v37, v26, v37
	v_fmac_f32_e32 v37, v16, v36
	v_fmac_f32_e32 v37, v17, v38
	v_fmac_f32_e32 v37, v19, v39
	v_add_f32_e32 v6, v6, v37
	ds_read_b128 v[36:39], v86 offset:5120
	global_store_dword v[80:81], v59, off offset:512
	global_store_dword v[80:81], v55, off offset:768
	global_store_dword v[80:81], v51, off offset:1024
	global_store_dword v[80:81], v47, off offset:1280
	s_waitcnt lgkmcnt(0)
	v_mul_f32_e32 v37, v18, v37
	v_fmac_f32_e32 v37, v12, v36
	v_fmac_f32_e32 v37, v13, v38
	v_fmac_f32_e32 v37, v15, v39
	v_add_f32_e32 v6, v6, v37
	ds_read_b128 v[36:39], v86 offset:6144
	global_store_dword v[80:81], v43, off offset:1536
	v_add_u32_e32 v240, s15, v68
	v_lshlrev_b32_e32 v236, 12, v240
	v_mov_b32_e32 v237, 0
	v_lshl_add_u64 v[236:237], v[70:71], 0, v[236:237]
	global_load_dwordx2 v[210:211], v[236:237], off
	global_load_dwordx2 v[212:213], v[236:237], off offset:3584
	global_load_dwordx2 v[214:215], v[236:237], off offset:512
	global_load_dwordx2 v[216:217], v[236:237], off offset:1024
	global_load_dwordx2 v[218:219], v[236:237], off offset:1536
	global_load_dwordx2 v[220:221], v[236:237], off offset:2048
	global_load_dwordx2 v[228:229], v[236:237], off offset:2560
	global_load_dwordx2 v[232:233], v[236:237], off offset:3072
	s_waitcnt lgkmcnt(0)
	v_mul_f32_e32 v37, v14, v37
	v_fmac_f32_e32 v37, v8, v36
	v_fmac_f32_e32 v37, v9, v38
	v_fmac_f32_e32 v37, v11, v39
	v_add_f32_e32 v6, v6, v37
	ds_read_b128 v[36:39], v86 offset:7168
	s_waitcnt lgkmcnt(0)
	v_mul_f32_e32 v37, v10, v37
	v_fmac_f32_e32 v37, v4, v36
	v_fmac_f32_e32 v37, v5, v38
	v_fmac_f32_e32 v37, v7, v39
	v_add_f32_e32 v6, v6, v37
	ds_read_b128 v[36:39], v86 offset:15360
	ds_read_b128 v[40:43], v86 offset:14336
	ds_read_b128 v[44:47], v86 offset:13312
	ds_read_b128 v[48:51], v86 offset:12288
	ds_read_b128 v[52:55], v86 offset:11264
	ds_read_b128 v[56:59], v86 offset:10240
	ds_read_b128 v[60:63], v86 offset:9216
	ds_read_b128 v[76:79], v86 offset:8192
	s_waitcnt lgkmcnt(4)
	v_mul_f32_e32 v49, v26, v49
	s_waitcnt lgkmcnt(3)
	v_mul_f32_e32 v53, v34, v53
	s_waitcnt lgkmcnt(2)
	v_mul_f32_e32 v57, v33, v57
	s_waitcnt lgkmcnt(1)
	v_mul_f32_e32 v61, v29, v61
	s_waitcnt lgkmcnt(0)
	v_mul_f32_e32 v65, v64, v77
	v_fmac_f32_e32 v65, v20, v76
	v_fmac_f32_e32 v65, v21, v78
	v_fmac_f32_e32 v61, v22, v60
	v_fmac_f32_e32 v65, v23, v79
	v_fmac_f32_e32 v61, v28, v62
	v_fmac_f32_e32 v57, v30, v56
	v_add_f32_e32 v65, 0, v65
	v_fmac_f32_e32 v61, v31, v63
	v_fmac_f32_e32 v57, v32, v58
	v_fmac_f32_e32 v53, v24, v52
	v_add_f32_e32 v60, v61, v65
	v_fmac_f32_e32 v57, v35, v59
	v_fmac_f32_e32 v53, v25, v54
	v_fmac_f32_e32 v49, v16, v48
	v_mul_f32_e32 v45, v18, v45
	v_add_f32_e32 v56, v57, v60
	v_fmac_f32_e32 v53, v27, v55
	v_fmac_f32_e32 v49, v17, v50
	v_fmac_f32_e32 v45, v12, v44
	v_mul_f32_e32 v41, v14, v41
	v_add_f32_e32 v52, v53, v56
	v_fmac_f32_e32 v49, v19, v51
	v_fmac_f32_e32 v45, v13, v46
	v_fmac_f32_e32 v41, v8, v40
	v_mul_f32_e32 v37, v10, v37
	v_add_f32_e32 v48, v49, v52
	v_fmac_f32_e32 v45, v15, v47
	v_fmac_f32_e32 v41, v9, v42
	v_fmac_f32_e32 v37, v4, v36
	v_add_f32_e32 v44, v45, v48
	v_fmac_f32_e32 v41, v11, v43
	v_fmac_f32_e32 v37, v5, v38
	v_add_f32_e32 v40, v41, v44
	v_fmac_f32_e32 v37, v7, v39
	v_add_f32_e32 v36, v37, v40
	ds_read_b128 v[38:41], v86 offset:23552
	ds_read_b128 v[42:45], v86 offset:22528
	ds_read_b128 v[46:49], v86 offset:21504
	ds_read_b128 v[50:53], v86 offset:20480
	ds_read_b128 v[54:57], v86 offset:19456
	ds_read_b128 v[58:61], v86 offset:18432
	ds_read_b128 v[76:79], v86 offset:17408
	ds_read_b128 v[152:155], v86 offset:16384
	s_waitcnt lgkmcnt(4)
	v_mul_f32_e32 v51, v26, v51
	s_waitcnt lgkmcnt(3)
	v_mul_f32_e32 v55, v34, v55
	s_waitcnt lgkmcnt(2)
	v_mul_f32_e32 v59, v33, v59
	s_waitcnt lgkmcnt(1)
	v_mul_f32_e32 v62, v29, v77
	s_waitcnt lgkmcnt(0)
	v_mul_f32_e32 v37, v64, v153
	v_fmac_f32_e32 v37, v20, v152
	v_fmac_f32_e32 v37, v21, v154
	v_fmac_f32_e32 v62, v22, v76
	v_fmac_f32_e32 v37, v23, v155
	v_fmac_f32_e32 v62, v28, v78
	v_fmac_f32_e32 v59, v30, v58
	v_add_f32_e32 v37, 0, v37
	v_fmac_f32_e32 v62, v31, v79
	v_fmac_f32_e32 v59, v32, v60
	v_fmac_f32_e32 v55, v24, v54
	v_add_f32_e32 v37, v62, v37
	v_fmac_f32_e32 v59, v35, v61
	v_fmac_f32_e32 v55, v25, v56
	v_fmac_f32_e32 v51, v16, v50
	v_mul_f32_e32 v47, v18, v47
	v_add_f32_e32 v37, v59, v37
	v_fmac_f32_e32 v55, v27, v57
	v_fmac_f32_e32 v51, v17, v52
	v_fmac_f32_e32 v47, v12, v46
	v_mul_f32_e32 v43, v14, v43
	v_add_f32_e32 v37, v55, v37
	v_fmac_f32_e32 v51, v19, v53
	v_fmac_f32_e32 v47, v13, v48
	v_fmac_f32_e32 v43, v8, v42
	v_mul_f32_e32 v39, v10, v39
	v_add_f32_e32 v37, v51, v37
	v_fmac_f32_e32 v47, v15, v49
	v_fmac_f32_e32 v43, v9, v44
	v_fmac_f32_e32 v39, v4, v38
	v_add_f32_e32 v37, v47, v37
	v_fmac_f32_e32 v43, v11, v45
	v_fmac_f32_e32 v39, v5, v40
	v_add_f32_e32 v37, v43, v37
	v_fmac_f32_e32 v39, v7, v41
	v_add_f32_e32 v37, v39, v37
	ds_read_b128 v[38:41], v86 offset:31744
	ds_read_b128 v[42:45], v86 offset:30720
	ds_read_b128 v[46:49], v86 offset:29696
	ds_read_b128 v[50:53], v86 offset:28672
	ds_read_b128 v[54:57], v86 offset:27648
	ds_read_b128 v[58:61], v86 offset:26624
	ds_read_b128 v[76:79], v86 offset:25600
	ds_read_b128 v[152:155], v86 offset:24576
	s_waitcnt lgkmcnt(4)
	v_mul_f32_e32 v51, v26, v51
	s_waitcnt lgkmcnt(3)
; template <int MODE>
; DEVI void phase_rows(const Params& p, int l, char* smem) {
;     ...
;             for (int e = 0; e < 16; ++e) { float t = 0.f;
; #pragma unroll
;                 for (int i = 0; i < 8; ++i) { const f32x4 w = *(const f32x4*)(wT + e * 2048 + i * 256 + lane * 4);
;                     t += v[i * 4] * w[0] + v[i * 4 + 1] * w[1] + v[i * 4 + 2] * w[2] + v[i * 4 + 3] * w[3]; }
;                 a[e] = t; if ((e & 3) == 3) __builtin_amdgcn_sched_barrier(0); }
	v_mul_f32_e32 v55, v34, v55
	s_waitcnt lgkmcnt(2)
	v_mul_f32_e32 v59, v33, v59
	s_waitcnt lgkmcnt(1)
	v_mul_f32_e32 v63, v29, v77
	s_waitcnt lgkmcnt(0)
	v_mul_f32_e32 v62, v64, v153
	v_fmac_f32_e32 v62, v20, v152
	v_fmac_f32_e32 v62, v21, v154
	v_fmac_f32_e32 v63, v22, v76
	v_fmac_f32_e32 v62, v23, v155
	v_fmac_f32_e32 v63, v28, v78
	v_fmac_f32_e32 v59, v30, v58
	v_add_f32_e32 v62, 0, v62
	v_fmac_f32_e32 v63, v31, v79
	v_fmac_f32_e32 v59, v32, v60
	v_fmac_f32_e32 v55, v24, v54
	v_add_f32_e32 v62, v63, v62
	v_fmac_f32_e32 v59, v35, v61
	v_fmac_f32_e32 v55, v25, v56
	v_fmac_f32_e32 v51, v16, v50
	v_mul_f32_e32 v47, v18, v47
	v_add_f32_e32 v58, v59, v62
	v_fmac_f32_e32 v55, v27, v57
	v_fmac_f32_e32 v51, v17, v52
	v_fmac_f32_e32 v47, v12, v46
	v_mul_f32_e32 v43, v14, v43
	v_add_f32_e32 v54, v55, v58
	v_fmac_f32_e32 v51, v19, v53
	v_fmac_f32_e32 v47, v13, v48
	v_fmac_f32_e32 v43, v8, v42
	v_mul_f32_e32 v39, v10, v39
	v_add_f32_e32 v50, v51, v54
	v_fmac_f32_e32 v47, v15, v49
	v_fmac_f32_e32 v43, v9, v44
	v_fmac_f32_e32 v39, v4, v38
	v_add_f32_e32 v46, v47, v50
	v_fmac_f32_e32 v43, v11, v45
	v_fmac_f32_e32 v39, v5, v40
	v_add_f32_e32 v42, v43, v46
	v_fmac_f32_e32 v39, v7, v41
	v_add_f32_e32 v38, v39, v42
	ds_read_b128 v[40:43], v86 offset:32768
	ds_read_b128 v[44:47], v86 offset:33792
	ds_read_b128 v[48:51], v86 offset:34816
	s_waitcnt lgkmcnt(2)
	v_mul_f32_e32 v39, v64, v41
	s_waitcnt lgkmcnt(1)
	v_mul_f32_e32 v41, v29, v45
	v_fmac_f32_e32 v39, v20, v40
	v_fmac_f32_e32 v41, v22, v44
	v_fmac_f32_e32 v39, v21, v42
	v_fmac_f32_e32 v39, v23, v43
	v_fmac_f32_e32 v41, v28, v46
	v_add_f32_e32 v39, 0, v39
	v_fmac_f32_e32 v41, v31, v47
	v_add_f32_e32 v39, v39, v41
	ds_read_b128 v[40:43], v86 offset:35840
	s_waitcnt lgkmcnt(1)
	v_mul_f32_e32 v44, v33, v49
	v_fmac_f32_e32 v44, v30, v48
	v_fmac_f32_e32 v44, v32, v50
	v_fmac_f32_e32 v44, v35, v51
	v_add_f32_e32 v39, v39, v44
	ds_read_b128 v[44:47], v86 offset:36864
	s_waitcnt lgkmcnt(1)
	v_mul_f32_e32 v41, v34, v41
	v_fmac_f32_e32 v41, v24, v40
	v_fmac_f32_e32 v41, v25, v42
	v_fmac_f32_e32 v41, v27, v43
	v_add_f32_e32 v39, v39, v41
	ds_read_b128 v[40:43], v86 offset:37888
	s_waitcnt lgkmcnt(1)
	v_mul_f32_e32 v45, v26, v45
	v_fmac_f32_e32 v45, v16, v44
	v_fmac_f32_e32 v45, v17, v46
	v_fmac_f32_e32 v45, v19, v47
	v_add_f32_e32 v39, v39, v45
	ds_read_b128 v[44:47], v86 offset:38912
	s_waitcnt lgkmcnt(1)
	v_mul_f32_e32 v41, v18, v41
	v_fmac_f32_e32 v41, v12, v40
	v_fmac_f32_e32 v41, v13, v42
	v_fmac_f32_e32 v41, v15, v43
	v_add_f32_e32 v39, v39, v41
	ds_read_b128 v[40:43], v86 offset:39936
	s_waitcnt lgkmcnt(1)
	v_mul_f32_e32 v45, v14, v45
	v_fmac_f32_e32 v45, v8, v44
	v_fmac_f32_e32 v45, v9, v46
	v_fmac_f32_e32 v45, v11, v47
	s_waitcnt lgkmcnt(0)
	v_mul_f32_e32 v41, v10, v41
	v_fmac_f32_e32 v41, v4, v40
	v_fmac_f32_e32 v41, v5, v42
	v_add_f32_e32 v39, v39, v45
	v_fmac_f32_e32 v41, v7, v43
	v_add_f32_e32 v39, v39, v41
	ds_read_b128 v[40:43], v86 offset:48128
	ds_read_b128 v[44:47], v86 offset:47104
	ds_read_b128 v[48:51], v86 offset:41984
	ds_read_b128 v[52:55], v86 offset:40960
	ds_read_b128 v[56:59], v86 offset:46080
	ds_read_b128 v[60:63], v86 offset:45056
	ds_read_b128 v[76:79], v86 offset:44032
	ds_read_b128 v[152:155], v86 offset:43008
	s_waitcnt lgkmcnt(4)
	v_mul_f32_e32 v53, v64, v53
	v_fmac_f32_e32 v53, v20, v52
	v_mul_f32_e32 v49, v29, v49
	v_fmac_f32_e32 v53, v21, v54
	v_fmac_f32_e32 v49, v22, v48
	v_fmac_f32_e32 v53, v23, v55
	v_fmac_f32_e32 v49, v28, v50
	v_add_f32_e32 v52, 0, v53
	v_fmac_f32_e32 v49, v31, v51
	v_add_f32_e32 v48, v49, v52
	s_waitcnt lgkmcnt(0)
	v_mul_f32_e32 v49, v33, v153
	v_fmac_f32_e32 v49, v30, v152
	v_fmac_f32_e32 v49, v32, v154
	v_fmac_f32_e32 v49, v35, v155
	v_add_f32_e32 v48, v49, v48
	v_mul_f32_e32 v49, v34, v77
	v_fmac_f32_e32 v49, v24, v76
	v_fmac_f32_e32 v49, v25, v78
	v_fmac_f32_e32 v49, v27, v79
	v_add_f32_e32 v48, v49, v48
	v_mul_f32_e32 v49, v26, v61
	v_fmac_f32_e32 v49, v16, v60
	v_fmac_f32_e32 v49, v17, v62
	v_fmac_f32_e32 v49, v19, v63
	v_add_f32_e32 v48, v49, v48
	v_mul_f32_e32 v49, v18, v57
	v_fmac_f32_e32 v49, v12, v56
	v_mul_f32_e32 v45, v14, v45
	v_fmac_f32_e32 v49, v13, v58
	v_fmac_f32_e32 v45, v8, v44
	v_mul_f32_e32 v41, v10, v41
	v_fmac_f32_e32 v49, v15, v59
	v_fmac_f32_e32 v45, v9, v46
	v_fmac_f32_e32 v41, v4, v40
	v_add_f32_e32 v48, v49, v48
	v_fmac_f32_e32 v45, v11, v47
	v_fmac_f32_e32 v41, v5, v42
	v_add_f32_e32 v44, v45, v48
	v_fmac_f32_e32 v41, v7, v43
	v_add_f32_e32 v40, v41, v44
	ds_read_b128 v[42:45], v86 offset:56320
	ds_read_b128 v[46:49], v86 offset:55296
	ds_read_b128 v[50:53], v86 offset:50176
	ds_read_b128 v[54:57], v86 offset:49152
	ds_read_b128 v[58:61], v86 offset:54272
	ds_read_b128 v[76:79], v86 offset:53248
	ds_read_b128 v[152:155], v86 offset:52224
	ds_read_b128 v[156:159], v86 offset:51200
	s_waitcnt lgkmcnt(4)
	v_mul_f32_e32 v41, v64, v55
	v_fmac_f32_e32 v41, v20, v54
	v_mul_f32_e32 v51, v29, v51
	v_fmac_f32_e32 v41, v21, v56
	v_fmac_f32_e32 v51, v22, v50
	s_waitcnt lgkmcnt(0)
; template <int MODE>
; DEVI void phase_rows(const Params& p, int l, char* smem) {
;     ...
;             for (int e = 0; e < 16; ++e) { float t = 0.f;
; #pragma unroll
;                 for (int i = 0; i < 8; ++i) { const f32x4 w = *(const f32x4*)(wT + e * 2048 + i * 256 + lane * 4);
;                     t += v[i * 4] * w[0] + v[i * 4 + 1] * w[1] + v[i * 4 + 2] * w[2] + v[i * 4 + 3] * w[3]; }
;                 a[e] = t; if ((e & 3) == 3) __builtin_amdgcn_sched_barrier(0); }
	v_mul_f32_e32 v50, v33, v157
	v_fmac_f32_e32 v41, v23, v57
	v_fmac_f32_e32 v51, v28, v52
	v_fmac_f32_e32 v50, v30, v156
	v_add_f32_e32 v41, 0, v41
	v_fmac_f32_e32 v51, v31, v53
	v_fmac_f32_e32 v50, v32, v158
	v_add_f32_e32 v41, v51, v41
	v_fmac_f32_e32 v50, v35, v159
	v_add_f32_e32 v41, v50, v41
	v_mul_f32_e32 v50, v34, v153
	v_fmac_f32_e32 v50, v24, v152
	v_fmac_f32_e32 v50, v25, v154
	v_fmac_f32_e32 v50, v27, v155
	v_add_f32_e32 v41, v50, v41
	v_mul_f32_e32 v50, v26, v77
	v_fmac_f32_e32 v50, v16, v76
	v_fmac_f32_e32 v50, v17, v78
	v_fmac_f32_e32 v50, v19, v79
	v_add_f32_e32 v41, v50, v41
	v_mul_f32_e32 v50, v18, v59
	v_fmac_f32_e32 v50, v12, v58
	v_mul_f32_e32 v47, v14, v47
	v_fmac_f32_e32 v50, v13, v60
	v_fmac_f32_e32 v47, v8, v46
	v_mul_f32_e32 v43, v10, v43
	v_fmac_f32_e32 v50, v15, v61
	v_fmac_f32_e32 v47, v9, v48
	v_fmac_f32_e32 v43, v4, v42
	v_add_f32_e32 v41, v50, v41
	v_fmac_f32_e32 v47, v11, v49
	v_fmac_f32_e32 v43, v5, v44
	v_add_f32_e32 v41, v47, v41
	v_fmac_f32_e32 v43, v7, v45
	v_add_f32_e32 v41, v43, v41
	ds_read_b128 v[42:45], v86 offset:64512
	ds_read_b128 v[46:49], v86 offset:63488
	ds_read_b128 v[50:53], v86 offset:58368
	ds_read_b128 v[54:57], v86 offset:57344
	ds_read_b128 v[58:61], v86 offset:62464
	ds_read_b128 v[76:79], v86 offset:61440
	ds_read_b128 v[152:155], v86 offset:60416
	ds_read_b128 v[156:159], v86 offset:59392
	s_waitcnt lgkmcnt(4)
	v_mul_f32_e32 v55, v64, v55
	v_fmac_f32_e32 v55, v20, v54
	v_mul_f32_e32 v51, v29, v51
	v_fmac_f32_e32 v55, v21, v56
	v_fmac_f32_e32 v51, v22, v50
	v_fmac_f32_e32 v55, v23, v57
	v_fmac_f32_e32 v51, v28, v52
	v_add_f32_e32 v54, 0, v55
	v_fmac_f32_e32 v51, v31, v53
	v_add_f32_e32 v50, v51, v54
	s_waitcnt lgkmcnt(0)
	v_mul_f32_e32 v51, v33, v157
	v_fmac_f32_e32 v51, v30, v156
	v_fmac_f32_e32 v51, v32, v158
	v_fmac_f32_e32 v51, v35, v159
	v_add_f32_e32 v50, v51, v50
	v_mul_f32_e32 v51, v34, v153
	v_fmac_f32_e32 v51, v24, v152
	v_fmac_f32_e32 v51, v25, v154
	v_fmac_f32_e32 v51, v27, v155
	v_add_f32_e32 v50, v51, v50
	v_mul_f32_e32 v51, v26, v77
	v_fmac_f32_e32 v51, v16, v76
	v_fmac_f32_e32 v51, v17, v78
	v_fmac_f32_e32 v51, v19, v79
	v_add_f32_e32 v50, v51, v50
	v_mul_f32_e32 v51, v18, v59
	v_fmac_f32_e32 v51, v12, v58
	v_mul_f32_e32 v47, v14, v47
	v_fmac_f32_e32 v51, v13, v60
	v_fmac_f32_e32 v47, v8, v46
	v_mul_f32_e32 v43, v10, v43
	v_fmac_f32_e32 v51, v15, v61
	v_fmac_f32_e32 v47, v9, v48
	v_fmac_f32_e32 v43, v4, v42
	v_add_f32_e32 v50, v51, v50
	v_fmac_f32_e32 v47, v11, v49
	v_fmac_f32_e32 v43, v5, v44
	v_add_f32_e32 v46, v47, v50
	v_fmac_f32_e32 v43, v7, v45
	v_add_f32_e32 v42, v43, v46
	ds_read_b128 v[44:47], v87
	ds_read_b128 v[48:51], v88
	ds_read_b128 v[52:55], v89
	s_waitcnt lgkmcnt(2)
	v_mul_f32_e32 v43, v64, v45
	s_waitcnt lgkmcnt(1)
	v_mul_f32_e32 v45, v29, v49
	v_fmac_f32_e32 v43, v20, v44
	v_fmac_f32_e32 v45, v22, v48
	v_fmac_f32_e32 v43, v21, v46
	v_fmac_f32_e32 v43, v23, v47
	v_fmac_f32_e32 v45, v28, v50
	v_add_f32_e32 v43, 0, v43
	v_fmac_f32_e32 v45, v31, v51
	v_add_f32_e32 v43, v43, v45
	ds_read_b128 v[44:47], v90
	s_waitcnt lgkmcnt(1)
	v_mul_f32_e32 v48, v33, v53
	v_fmac_f32_e32 v48, v30, v52
	v_fmac_f32_e32 v48, v32, v54
	v_fmac_f32_e32 v48, v35, v55
	v_add_f32_e32 v43, v43, v48
	ds_read_b128 v[48:51], v91
	s_waitcnt lgkmcnt(1)
	v_mul_f32_e32 v45, v34, v45
	v_fmac_f32_e32 v45, v24, v44
	v_fmac_f32_e32 v45, v25, v46
	v_fmac_f32_e32 v45, v27, v47
	v_add_f32_e32 v43, v43, v45
	ds_read_b128 v[44:47], v92
	s_waitcnt lgkmcnt(1)
	v_mul_f32_e32 v49, v26, v49
	v_fmac_f32_e32 v49, v16, v48
	v_fmac_f32_e32 v49, v17, v50
	v_fmac_f32_e32 v49, v19, v51
	v_add_f32_e32 v43, v43, v49
	ds_read_b128 v[48:51], v93
	s_waitcnt lgkmcnt(1)
	v_mul_f32_e32 v45, v18, v45
	v_fmac_f32_e32 v45, v12, v44
	v_fmac_f32_e32 v45, v13, v46
	v_fmac_f32_e32 v45, v15, v47
	v_add_f32_e32 v43, v43, v45
	ds_read_b128 v[44:47], v94
	s_waitcnt lgkmcnt(1)
	v_mul_f32_e32 v49, v14, v49
	v_fmac_f32_e32 v49, v8, v48
	v_fmac_f32_e32 v49, v9, v50
	v_fmac_f32_e32 v49, v11, v51
	s_waitcnt lgkmcnt(0)
	v_mul_f32_e32 v45, v10, v45
	v_fmac_f32_e32 v45, v4, v44
	v_fmac_f32_e32 v45, v5, v46
	v_add_f32_e32 v43, v43, v49
	v_fmac_f32_e32 v45, v7, v47
	v_add_f32_e32 v43, v43, v45
	ds_read_b128 v[44:47], v97
	ds_read_b128 v[48:51], v98
	ds_read_b128 v[52:55], v95
	ds_read_b128 v[56:59], v96
	ds_read_b128 v[60:63], v99
	ds_read_b128 v[76:79], v100
	ds_read_b128 v[152:155], v101
	ds_read_b128 v[156:159], v102
	s_waitcnt lgkmcnt(4)
	v_mul_f32_e32 v57, v64, v57
	v_fmac_f32_e32 v57, v20, v56
	v_fmac_f32_e32 v57, v21, v58
	v_fmac_f32_e32 v57, v23, v59
	v_add_f32_e32 v56, 0, v57
	s_waitcnt lgkmcnt(0)
	v_mul_f32_e32 v57, v29, v157
	v_fmac_f32_e32 v57, v22, v156
	v_fmac_f32_e32 v57, v28, v158
	v_fmac_f32_e32 v57, v31, v159
	v_add_f32_e32 v56, v57, v56
	v_mul_f32_e32 v57, v33, v153
	v_fmac_f32_e32 v57, v30, v152
	v_fmac_f32_e32 v57, v32, v154
	v_fmac_f32_e32 v57, v35, v155
	v_add_f32_e32 v56, v57, v56
	v_mul_f32_e32 v57, v34, v77
	v_fmac_f32_e32 v57, v24, v76
	v_fmac_f32_e32 v57, v25, v78
	v_fmac_f32_e32 v57, v27, v79
	v_add_f32_e32 v56, v57, v56
	v_mul_f32_e32 v57, v26, v61
	v_fmac_f32_e32 v57, v16, v60
	v_mul_f32_e32 v49, v18, v49
	v_fmac_f32_e32 v57, v17, v62
	v_fmac_f32_e32 v49, v12, v48
	v_mul_f32_e32 v45, v14, v45
	v_fmac_f32_e32 v57, v19, v63
	v_fmac_f32_e32 v49, v13, v50
	v_fmac_f32_e32 v45, v8, v44
	v_add_f32_e32 v56, v57, v56
	v_fmac_f32_e32 v49, v15, v51
	v_fmac_f32_e32 v45, v9, v46
	v_add_f32_e32 v48, v49, v56
	v_fmac_f32_e32 v45, v11, v47
	v_add_f32_e32 v44, v45, v48
	v_mul_f32_e32 v45, v10, v53
	v_fmac_f32_e32 v45, v4, v52
	v_fmac_f32_e32 v45, v5, v54
	v_fmac_f32_e32 v45, v7, v55
	v_add_f32_e32 v65, v45, v44
	ds_read_b128 v[44:47], v105
	ds_read_b128 v[48:51], v106
	ds_read_b128 v[52:55], v103
	ds_read_b128 v[56:59], v104
	ds_read_b128 v[60:63], v107
	ds_read_b128 v[76:79], v108
	ds_read_b128 v[152:155], v109
	ds_read_b128 v[156:159], v110
	s_waitcnt lgkmcnt(4)
; template <int MODE>
; DEVI void phase_rows(const Params& p, int l, char* smem) {
;     ...
;             for (int e = 0; e < 16; ++e) { float t = 0.f;
; #pragma unroll
;                 for (int i = 0; i < 8; ++i) { const f32x4 w = *(const f32x4*)(wT + e * 2048 + i * 256 + lane * 4);
;                     t += v[i * 4] * w[0] + v[i * 4 + 1] * w[1] + v[i * 4 + 2] * w[2] + v[i * 4 + 3] * w[3]; }
;                 a[e] = t; if ((e & 3) == 3) __builtin_amdgcn_sched_barrier(0); }
	v_mul_f32_e32 v57, v64, v57
	v_fmac_f32_e32 v57, v20, v56
	v_fmac_f32_e32 v57, v21, v58
	v_fmac_f32_e32 v57, v23, v59
	v_add_f32_e32 v56, 0, v57
	s_waitcnt lgkmcnt(0)
	v_mul_f32_e32 v57, v29, v157
	v_fmac_f32_e32 v57, v22, v156
	v_fmac_f32_e32 v57, v28, v158
	v_fmac_f32_e32 v57, v31, v159
	v_add_f32_e32 v56, v57, v56
	v_mul_f32_e32 v57, v33, v153
	v_fmac_f32_e32 v57, v30, v152
	v_fmac_f32_e32 v57, v32, v154
	v_fmac_f32_e32 v57, v35, v155
	v_add_f32_e32 v56, v57, v56
	v_mul_f32_e32 v57, v34, v77
	v_fmac_f32_e32 v57, v24, v76
	v_fmac_f32_e32 v57, v25, v78
	v_fmac_f32_e32 v57, v27, v79
	v_add_f32_e32 v56, v57, v56
	v_mul_f32_e32 v57, v26, v61
	v_fmac_f32_e32 v57, v16, v60
	v_mul_f32_e32 v49, v18, v49
	v_fmac_f32_e32 v57, v17, v62
	v_fmac_f32_e32 v49, v12, v48
	v_mul_f32_e32 v45, v14, v45
	v_fmac_f32_e32 v57, v19, v63
	v_fmac_f32_e32 v49, v13, v50
	v_fmac_f32_e32 v45, v8, v44
	v_add_f32_e32 v56, v57, v56
	v_fmac_f32_e32 v49, v15, v51
	v_fmac_f32_e32 v45, v9, v46
	v_add_f32_e32 v48, v49, v56
	v_fmac_f32_e32 v45, v11, v47
	v_add_f32_e32 v44, v45, v48
	v_mul_f32_e32 v45, v10, v53
	v_fmac_f32_e32 v45, v4, v52
	v_fmac_f32_e32 v45, v5, v54
	v_fmac_f32_e32 v45, v7, v55
	v_add_f32_e32 v66, v45, v44
	ds_read_b128 v[44:47], v113
	ds_read_b128 v[48:51], v114
	ds_read_b128 v[52:55], v111
	ds_read_b128 v[56:59], v112
	ds_read_b128 v[60:63], v115
	ds_read_b128 v[76:79], v116
	ds_read_b128 v[152:155], v117
	ds_read_b128 v[156:159], v118
	s_waitcnt lgkmcnt(4)
	v_mul_f32_e32 v57, v64, v57
	v_fmac_f32_e32 v57, v20, v56
	v_fmac_f32_e32 v57, v21, v58
	v_fmac_f32_e32 v57, v23, v59
	v_add_f32_e32 v56, 0, v57
	s_waitcnt lgkmcnt(0)
	v_mul_f32_e32 v57, v29, v157
	v_fmac_f32_e32 v57, v22, v156
	v_fmac_f32_e32 v57, v28, v158
	v_fmac_f32_e32 v57, v31, v159
	v_add_f32_e32 v56, v57, v56
	v_mul_f32_e32 v57, v33, v153
	v_fmac_f32_e32 v57, v30, v152
	v_fmac_f32_e32 v57, v32, v154
	v_fmac_f32_e32 v57, v35, v155
	v_add_f32_e32 v56, v57, v56
	v_mul_f32_e32 v57, v34, v77
	v_fmac_f32_e32 v57, v24, v76
	v_fmac_f32_e32 v57, v25, v78
	v_fmac_f32_e32 v57, v27, v79
	v_add_f32_e32 v56, v57, v56
	v_mul_f32_e32 v57, v26, v61
	v_fmac_f32_e32 v57, v16, v60
	v_mul_f32_e32 v49, v18, v49
	v_fmac_f32_e32 v57, v17, v62
	v_fmac_f32_e32 v49, v12, v48
	v_mul_f32_e32 v45, v14, v45
	v_fmac_f32_e32 v57, v19, v63
	v_fmac_f32_e32 v49, v13, v50
	v_fmac_f32_e32 v45, v8, v44
	v_add_f32_e32 v56, v57, v56
	v_fmac_f32_e32 v49, v15, v51
	v_fmac_f32_e32 v45, v9, v46
	v_add_f32_e32 v48, v49, v56
	v_fmac_f32_e32 v45, v11, v47
	v_add_f32_e32 v44, v45, v48
	v_mul_f32_e32 v45, v10, v53
	v_fmac_f32_e32 v45, v4, v52
	v_fmac_f32_e32 v45, v5, v54
	v_fmac_f32_e32 v45, v7, v55
	v_add_f32_e32 v67, v45, v44
	ds_read_b128 v[44:47], v119
	ds_read_b128 v[48:51], v120
	ds_read_b128 v[52:55], v121
	s_waitcnt lgkmcnt(2)
	v_mul_f32_e32 v45, v64, v45
	s_waitcnt lgkmcnt(1)
	v_mul_f32_e32 v49, v29, v49
	v_fmac_f32_e32 v45, v20, v44
	v_fmac_f32_e32 v49, v22, v48
	v_fmac_f32_e32 v45, v21, v46
	v_fmac_f32_e32 v45, v23, v47
	v_fmac_f32_e32 v49, v28, v50
	v_add_f32_e32 v44, 0, v45
	v_fmac_f32_e32 v49, v31, v51
	v_add_f32_e32 v48, v44, v49
	ds_read_b128 v[44:47], v122
	s_waitcnt lgkmcnt(1)
	v_mul_f32_e32 v49, v33, v53
	v_fmac_f32_e32 v49, v30, v52
	v_fmac_f32_e32 v49, v32, v54
	v_fmac_f32_e32 v49, v35, v55
	v_add_f32_e32 v52, v48, v49
	ds_read_b128 v[48:51], v123
	s_waitcnt lgkmcnt(1)
	v_mul_f32_e32 v45, v34, v45
	v_fmac_f32_e32 v45, v24, v44
	v_fmac_f32_e32 v45, v25, v46
	v_fmac_f32_e32 v45, v27, v47
	v_add_f32_e32 v52, v52, v45
	ds_read_b128 v[44:47], v124
	s_waitcnt lgkmcnt(1)
	v_mul_f32_e32 v49, v26, v49
	v_fmac_f32_e32 v49, v16, v48
	v_fmac_f32_e32 v49, v17, v50
	v_fmac_f32_e32 v49, v19, v51
	v_add_f32_e32 v52, v52, v49
	ds_read_b128 v[48:51], v125
	s_waitcnt lgkmcnt(1)
	v_mul_f32_e32 v45, v18, v45
	v_fmac_f32_e32 v45, v12, v44
	v_fmac_f32_e32 v45, v13, v46
	v_fmac_f32_e32 v45, v15, v47
	v_add_f32_e32 v52, v52, v45
	ds_read_b128 v[44:47], v126
	s_waitcnt lgkmcnt(1)
	v_mul_f32_e32 v49, v14, v49
	v_fmac_f32_e32 v49, v8, v48
	v_fmac_f32_e32 v49, v9, v50
	v_fmac_f32_e32 v49, v11, v51
	s_waitcnt lgkmcnt(0)
	v_mul_f32_e32 v45, v10, v45
	v_fmac_f32_e32 v45, v4, v44
	v_fmac_f32_e32 v45, v5, v46
	v_add_f32_e32 v48, v52, v49
	v_fmac_f32_e32 v45, v7, v47
	v_add_f32_e32 v69, v48, v45
	ds_read_b128 v[44:47], v129
	ds_read_b128 v[48:51], v130
	ds_read_b128 v[52:55], v127
	ds_read_b128 v[56:59], v128
	ds_read_b128 v[60:63], v131
	ds_read_b128 v[76:79], v132
	ds_read_b128 v[152:155], v133
	ds_read_b128 v[156:159], v134
	s_waitcnt lgkmcnt(4)
	v_mul_f32_e32 v57, v64, v57
	v_fmac_f32_e32 v57, v20, v56
	v_fmac_f32_e32 v57, v21, v58
	v_fmac_f32_e32 v57, v23, v59
	v_add_f32_e32 v56, 0, v57
	s_waitcnt lgkmcnt(0)
	v_mul_f32_e32 v57, v29, v157
	v_fmac_f32_e32 v57, v22, v156
	v_fmac_f32_e32 v57, v28, v158
	v_fmac_f32_e32 v57, v31, v159
	v_add_f32_e32 v56, v57, v56
	v_mul_f32_e32 v57, v33, v153
	v_fmac_f32_e32 v57, v30, v152
	v_fmac_f32_e32 v57, v32, v154
	v_fmac_f32_e32 v57, v35, v155
	v_add_f32_e32 v56, v57, v56
	v_mul_f32_e32 v57, v34, v77
	v_fmac_f32_e32 v57, v24, v76
	v_fmac_f32_e32 v57, v25, v78
	v_fmac_f32_e32 v57, v27, v79
	v_add_f32_e32 v56, v57, v56
	v_mul_f32_e32 v57, v26, v61
	v_fmac_f32_e32 v57, v16, v60
	v_mul_f32_e32 v49, v18, v49
	v_fmac_f32_e32 v57, v17, v62
	v_fmac_f32_e32 v49, v12, v48
	v_mul_f32_e32 v45, v14, v45
	v_fmac_f32_e32 v57, v19, v63
	v_fmac_f32_e32 v49, v13, v50
	v_fmac_f32_e32 v45, v8, v44
	v_add_f32_e32 v56, v57, v56
	v_fmac_f32_e32 v49, v15, v51
	v_fmac_f32_e32 v45, v9, v46
	v_add_f32_e32 v48, v49, v56
	v_fmac_f32_e32 v45, v11, v47
	v_add_f32_e32 v44, v45, v48
	v_mul_f32_e32 v45, v10, v53
	v_fmac_f32_e32 v45, v4, v52
	v_fmac_f32_e32 v45, v5, v54
	v_fmac_f32_e32 v45, v7, v55
	v_add_f32_e32 v80, v45, v44
	ds_read_b128 v[44:47], v137
	ds_read_b128 v[48:51], v138
	ds_read_b128 v[52:55], v135
	ds_read_b128 v[56:59], v136
	ds_read_b128 v[60:63], v139
	ds_read_b128 v[76:79], v140
	ds_read_b128 v[152:155], v141
	ds_read_b128 v[156:159], v142
	s_waitcnt lgkmcnt(4)
; template <int MODE>
; DEVI void phase_rows(const Params& p, int l, char* smem) {
;     ...
;             const bool b5 = (lane & 32) != 0, b4 = (lane & 16) != 0, b3 = (lane & 8) != 0, b2 = (lane & 4) != 0;
;             float s8[8], s4[4], s2[2], s1;
; #pragma unroll
;             for (int i = 0; i < 8; ++i) { const float keep = b5 ? a[8 + i] : a[i], give = b5 ? a[i] : a[8 + i]; s8[i] = keep + __shfl_xor(give, 32); }
; #pragma unroll
;             for (int i = 0; i < 4; ++i) { const float keep = b4 ? s8[4 + i] : s8[i], give = b4 ? s8[i] : s8[4 + i]; s4[i] = keep + __shfl_xor(give, 16); }
; #pragma unroll
;             for (int i = 0; i < 2; ++i) { const float keep = b3 ? s4[2 + i] : s4[i], give = b3 ? s4[i] : s4[2 + i]; s2[i] = keep + __shfl_xor(give, 8); }
;             { const float keep = b2 ? s2[1] : s2[0], give = b2 ? s2[0] : s2[1]; s1 = keep + __shfl_xor(give, 4); }
;             s1 += __shfl_xor(s1, 2); s1 += __shfl_xor(s1, 1);
;             float mx = s1;
; #pragma unroll
;             for (int off = 32; off >= 4; off >>= 1) mx = fmaxf(mx, __shfl_xor(mx, off));
;             const float ex = expf(s1 - mx); float den = ex;
; #pragma unroll
;             for (int off = 32; off >= 4; off >>= 1) den += __shfl_xor(den, off);
;             const int eidx = (b5 ? 8 : 0) + (b4 ? 4 : 0) + (b3 ? 2 : 0) + (b2 ? 1 : 0);
	v_mul_f32_e32 v57, v64, v57
	v_fmac_f32_e32 v57, v20, v56
	v_fmac_f32_e32 v57, v21, v58
	v_fmac_f32_e32 v57, v23, v59
	v_add_f32_e32 v56, 0, v57
	s_waitcnt lgkmcnt(0)
	v_mul_f32_e32 v57, v29, v157
	v_fmac_f32_e32 v57, v22, v156
	v_fmac_f32_e32 v57, v28, v158
	v_fmac_f32_e32 v57, v31, v159
	v_add_f32_e32 v56, v57, v56
	v_mul_f32_e32 v57, v33, v153
	v_fmac_f32_e32 v57, v30, v152
	v_fmac_f32_e32 v57, v32, v154
	v_fmac_f32_e32 v57, v35, v155
	v_add_f32_e32 v56, v57, v56
	v_mul_f32_e32 v57, v34, v77
	v_fmac_f32_e32 v57, v24, v76
	v_fmac_f32_e32 v57, v25, v78
	v_fmac_f32_e32 v57, v27, v79
	v_add_f32_e32 v56, v57, v56
	v_mul_f32_e32 v57, v26, v61
	v_fmac_f32_e32 v57, v16, v60
	v_mul_f32_e32 v49, v18, v49
	v_fmac_f32_e32 v57, v17, v62
	v_fmac_f32_e32 v49, v12, v48
	v_mul_f32_e32 v45, v14, v45
	v_fmac_f32_e32 v57, v19, v63
	v_fmac_f32_e32 v49, v13, v50
	v_fmac_f32_e32 v45, v8, v44
	v_add_f32_e32 v56, v57, v56
	v_fmac_f32_e32 v49, v15, v51
	v_fmac_f32_e32 v45, v9, v46
	v_add_f32_e32 v48, v49, v56
	v_fmac_f32_e32 v45, v11, v47
	v_add_f32_e32 v44, v45, v48
	v_mul_f32_e32 v45, v10, v53
	v_fmac_f32_e32 v45, v4, v52
	v_fmac_f32_e32 v45, v5, v54
	v_fmac_f32_e32 v45, v7, v55
	v_add_f32_e32 v81, v45, v44
	ds_read_b128 v[44:47], v145
	ds_read_b128 v[48:51], v146
	ds_read_b128 v[52:55], v143
	ds_read_b128 v[56:59], v144
	ds_read_b128 v[60:63], v147
	ds_read_b128 v[76:79], v148
	ds_read_b128 v[152:155], v149
	ds_read_b128 v[156:159], v150
	s_waitcnt lgkmcnt(4)
	v_mul_f32_e32 v57, v64, v57
	v_fmac_f32_e32 v57, v20, v56
	v_fmac_f32_e32 v57, v21, v58
	v_fmac_f32_e32 v57, v23, v59
	s_waitcnt lgkmcnt(0)
	v_mul_f32_e32 v21, v29, v157
	v_fmac_f32_e32 v21, v22, v156
	v_fmac_f32_e32 v21, v28, v158
	v_add_f32_e32 v20, 0, v57
	v_fmac_f32_e32 v21, v31, v159
	v_add_f32_e32 v20, v21, v20
	v_mul_f32_e32 v21, v33, v153
	v_fmac_f32_e32 v21, v30, v152
	v_fmac_f32_e32 v21, v32, v154
	v_fmac_f32_e32 v21, v35, v155
	v_add_f32_e32 v20, v21, v20
	v_mul_f32_e32 v21, v34, v77
	v_fmac_f32_e32 v21, v24, v76
	v_fmac_f32_e32 v21, v25, v78
	v_fmac_f32_e32 v21, v27, v79
	v_add_f32_e32 v20, v21, v20
	v_mul_f32_e32 v21, v26, v61
	v_fmac_f32_e32 v21, v16, v60
	v_fmac_f32_e32 v21, v17, v62
	v_mul_f32_e32 v17, v18, v49
	v_fmac_f32_e32 v17, v12, v48
	v_fmac_f32_e32 v17, v13, v50
	v_mul_f32_e32 v13, v14, v45
	v_fmac_f32_e32 v13, v8, v44
	v_fmac_f32_e32 v21, v19, v63
	v_fmac_f32_e32 v13, v9, v46
	v_mul_f32_e32 v9, v10, v53
	v_add_f32_e32 v16, v21, v20
	v_fmac_f32_e32 v17, v15, v51
	v_fmac_f32_e32 v9, v4, v52
	v_add_f32_e32 v12, v17, v16
	v_fmac_f32_e32 v13, v11, v47
	v_fmac_f32_e32 v9, v5, v54
	v_add_f32_e32 v8, v13, v12
	v_fmac_f32_e32 v9, v7, v55
	v_add_f32_e32 v4, v9, v8
	v_cndmask_b32_e64 v5, v43, v6, s[38:39]
	v_cndmask_b32_e64 v6, v6, v43, s[38:39]
	ds_bpermute_b32 v6, v1, v6
	v_cndmask_b32_e64 v7, v36, v65, s[38:39]
	ds_bpermute_b32 v7, v1, v7
	v_cndmask_b32_e64 v8, v37, v66, s[38:39]
	ds_bpermute_b32 v8, v1, v8
	v_cndmask_b32_e64 v9, v38, v67, s[38:39]
	ds_bpermute_b32 v9, v1, v9
	v_cndmask_b32_e64 v10, v39, v69, s[38:39]
	ds_bpermute_b32 v10, v1, v10
	v_cndmask_b32_e64 v11, v40, v80, s[38:39]
	s_waitcnt lgkmcnt(4)
	v_add_f32_e32 v5, v5, v6
	v_cndmask_b32_e64 v6, v65, v36, s[38:39]
	ds_bpermute_b32 v11, v1, v11
	v_cndmask_b32_e64 v12, v41, v81, s[38:39]
	s_waitcnt lgkmcnt(4)
	v_add_f32_e32 v6, v6, v7
	v_cndmask_b32_e64 v7, v66, v37, s[38:39]
	ds_bpermute_b32 v12, v1, v12
	s_waitcnt lgkmcnt(4)
	v_add_f32_e32 v7, v7, v8
	v_cndmask_b32_e64 v8, v67, v38, s[38:39]
	s_waitcnt lgkmcnt(3)
	v_add_f32_e32 v8, v8, v9
	v_cndmask_b32_e64 v9, v69, v39, s[38:39]
	s_waitcnt lgkmcnt(2)
	v_add_f32_e32 v9, v9, v10
	v_cndmask_b32_e64 v10, v80, v40, s[38:39]
	s_waitcnt lgkmcnt(1)
	v_add_f32_e32 v10, v10, v11
	v_cndmask_b32_e64 v11, v81, v41, s[38:39]
	s_waitcnt lgkmcnt(0)
	v_add_f32_e32 v11, v11, v12
	v_cndmask_b32_e64 v12, v4, v42, s[38:39]
	v_cndmask_b32_e64 v4, v42, v4, s[38:39]
	ds_bpermute_b32 v4, v1, v4
	s_mov_b32 s4, 0xc2ce8ed0
	s_waitcnt lgkmcnt(0)
	v_add_f32_e32 v4, v12, v4
	v_cndmask_b32_e64 v12, v9, v5, s[40:41]
	v_cndmask_b32_e64 v5, v5, v9, s[40:41]
	v_cndmask_b32_e64 v9, v10, v6, s[40:41]
	v_cndmask_b32_e64 v6, v6, v10, s[40:41]
	ds_bpermute_b32 v6, v75, v6
	ds_bpermute_b32 v5, v75, v5
	s_waitcnt lgkmcnt(1)
	v_add_f32_e32 v6, v9, v6
	v_cndmask_b32_e64 v9, v11, v7, s[40:41]
	v_cndmask_b32_e64 v7, v7, v11, s[40:41]
	ds_bpermute_b32 v7, v75, v7
	s_waitcnt lgkmcnt(1)
	v_add_f32_e32 v5, v12, v5
	s_waitcnt lgkmcnt(0)
	v_add_f32_e32 v7, v9, v7
	v_cndmask_b32_e64 v9, v4, v8, s[40:41]
	v_cndmask_b32_e64 v4, v8, v4, s[40:41]
	ds_bpermute_b32 v4, v75, v4
	v_cndmask_b32_e64 v8, v7, v5, s[42:43]
	v_cndmask_b32_e64 v5, v5, v7, s[42:43]
	ds_bpermute_b32 v5, v82, v5
	s_waitcnt lgkmcnt(1)
	v_add_f32_e32 v4, v9, v4
	v_cndmask_b32_e64 v7, v4, v6, s[42:43]
	v_cndmask_b32_e64 v4, v6, v4, s[42:43]
	ds_bpermute_b32 v4, v82, v4
	s_waitcnt lgkmcnt(1)
	v_add_f32_e32 v5, v8, v5
	s_waitcnt lgkmcnt(0)
	v_add_f32_e32 v4, v7, v4
	v_cndmask_b32_e64 v6, v4, v5, s[44:45]
	v_cndmask_b32_e64 v4, v5, v4, s[44:45]
	ds_bpermute_b32 v4, v83, v4
	s_waitcnt lgkmcnt(0)
	v_add_f32_e32 v4, v6, v4
	ds_bpermute_b32 v5, v84, v4
	s_waitcnt lgkmcnt(0)
	v_add_f32_e32 v4, v4, v5
	ds_bpermute_b32 v5, v85, v4
	s_waitcnt lgkmcnt(0)
	v_add_f32_e32 v4, v4, v5
	ds_bpermute_b32 v5, v1, v4
	s_waitcnt lgkmcnt(0)
	v_max_f32_e32 v5, v5, v5
	v_max_f32_e32 v5, v4, v5
	ds_bpermute_b32 v6, v75, v5
	s_waitcnt lgkmcnt(0)
	v_max_f32_e32 v6, v6, v6
	v_max_f32_e32 v5, v5, v6
	ds_bpermute_b32 v6, v82, v5
	s_waitcnt lgkmcnt(0)
	v_max_f32_e32 v6, v6, v6
	v_max_f32_e32 v5, v5, v6
	ds_bpermute_b32 v6, v83, v5
	s_waitcnt lgkmcnt(0)
	v_max_f32_e32 v6, v6, v6
	v_max_f32_e32 v5, v5, v6
	v_sub_f32_e32 v4, v4, v5
	v_mul_f32_e32 v5, 0x3fb8aa3b, v4
	v_fma_f32 v6, v4, s72, -v5
	v_rndne_f32_e32 v7, v5
	v_fmac_f32_e32 v6, 0x32a5705f, v4
	v_sub_f32_e32 v5, v5, v7
	v_add_f32_e32 v5, v5, v6
	v_exp_f32_e32 v5, v5
	v_cvt_i32_f32_e32 v6, v7
	v_cmp_ngt_f32_e64 s[50:51], s4, v4
	s_mov_b32 s4, 0x42b17218
	v_ldexp_f32 v5, v5, v6
	v_cndmask_b32_e64 v5, 0, v5, s[50:51]
	v_cmp_nlt_f32_e64 s[50:51], s4, v4
	v_mov_b32_e32 v4, 0x7f800000
	s_nop 0
	v_cndmask_b32_e64 v4, v4, v5, s[50:51]
	ds_bpermute_b32 v5, v1, v4
	s_waitcnt lgkmcnt(0)
	v_add_f32_e32 v5, v4, v5
	ds_bpermute_b32 v6, v75, v5
	s_waitcnt lgkmcnt(0)
	v_add_f32_e32 v5, v5, v6
	ds_bpermute_b32 v6, v82, v5
	s_waitcnt lgkmcnt(0)
	v_add_f32_e32 v5, v5, v6
	ds_bpermute_b32 v6, v83, v5
	s_and_saveexec_b64 s[16:17], s[46:47]
	s_cbranch_execz .LBB0_1042
; template <int MODE>
; DEVI void phase_rows(const Params& p, int l, char* smem) {
;     ...
;             const float ex = expf(s1 - mx); float den = ex;
; #pragma unroll
;             for (int off = 32; off >= 4; off >>= 1) den += __shfl_xor(den, off);
;             const int eidx = (b5 ? 8 : 0) + (b4 ? 4 : 0) + (b3 ? 2 : 0) + (b2 ? 1 : 0);
;             if ((lane & 3) == 0) ((float*)(p.ws + WS_AFF))[((size_t)b * 16 + eidx) * KEYS + tok] = ex / den;
	s_movk_i32 s4, 0x800
	s_waitcnt lgkmcnt(0)
	v_add_f32_e32 v5, v5, v6
	v_and_b32_e32 v7, 0x7ff, v68
	v_or_b32_sdwa v8, v68, s4 dst_sel:DWORD dst_unused:UNUSED_PAD src0_sel:BYTE_0 src1_sel:DWORD
	v_div_scale_f32 v6, s[4:5], v5, v5, v4
	v_cndmask_b32_e32 v7, v8, v7, vcc
	v_rcp_f32_e32 v8, v6
	v_add_u32_e32 v9, 0xffffe000, v68
	v_lshrrev_b32_e32 v9, 8, v9
	v_cndmask_b32_e32 v9, v9, v151, vcc
	v_fma_f32 v10, -v6, v8, 1.0
	v_fmac_f32_e32 v8, v10, v8
	v_div_scale_f32 v10, vcc, v4, v5, v4
	v_mul_f32_e32 v11, v10, v8
	v_fma_f32 v12, -v6, v11, v10
	v_fmac_f32_e32 v11, v12, v8
	v_fma_f32 v6, -v6, v11, v10
	v_div_fmas_f32 v6, v6, v8, v11
	v_div_fixup_f32 v8, v6, v5, v4
	v_lshl_or_b32 v6, v9, 4, v74
	v_mov_b64_e32 v[4:5], s[6:7]
	s_movk_i32 s4, 0x2400
	v_mad_i64_i32 v[4:5], s[4:5], v6, s4, v[4:5]
	v_lshlrev_b32_e32 v6, 2, v7
	v_mov_b32_e32 v7, v3
	v_lshl_add_u64 v[4:5], v[4:5], 0, v[6:7]
	global_store_dword v[4:5], v8, off
	s_branch .LBB0_1042
